# v039 + topk first-half score MFMAs: rolling window of 16 LDS fragment reads, k-step-major MFMA order (no per-MFMA lgkmcnt(0) ladder)
# speedup vs baseline: 1.0088x; 1.0010x over previous
; #define LAS __attribute__((address_space(3)))
; __device__ __forceinline__ f32x4 mfma16(bf16x8 a, bf16x8 b, f32x4 c) { return __builtin_amdgcn_mfma_f32_16x16x32_bf16(a, b, c, 0, 0, 0); }
; __device__ __forceinline__ void topk_phase(LAS unsigned char* lds, const bf16_t* qp, const bf16_t* keys, const float* SU, const float* SV, int* sel_e, float* sel_g, float* sel_su, int G, int b) {
;     ...
;         for (int p = 0; p < 2; ++p) {
;             f32x4 acc[8];
; #pragma unroll
;             for (int mt = 0; mt < 8; ++mt) acc[mt] = (f32x4){0.f, 0.f, 0.f, 0.f};
;             bf16x8 bq[4];
; #pragma unroll
;             for (int ks = 0; ks < 4; ++ks) bq[ks] = *(const bf16x8*)(qp + (size_t)tok * D_ + h * 256 + p * 128 + ks * 32 + fq * 8);
;             const LAS bf16_t* kb = KL + p * 128 * 136;
; #pragma unroll
;             for (int mt = 0; mt < 8; ++mt)
; #pragma unroll
;                 for (int ks = 0; ks < 4; ++ks) { const bf16x8 a = *(const LAS bf16x8*)(kb + (mt * 16 + fr) * 136 + ks * 32 + fq * 8); acc[mt] = mfma16(a, bq[ks], acc[mt]); }
.LBB0_659:
	s_and_b32 s0, s52, 1
	s_lshl_b32 s1, s64, 8
	s_lshl_b32 s0, s0, 7
	s_or_b32 s0, s1, s0
	v_add_u32_e32 v94, s0, v85
	v_ashrrev_i32_e32 v95, 31, v94
	v_lshlrev_b64 v[34:35], 12, v[94:95]
	s_lshl_b32 s0, s56, 8
	v_lshl_add_u64 v[34:35], s[74:75], 0, v[34:35]
	s_ashr_i32 s1, s0, 31
	v_lshl_add_u64 v[34:35], s[0:1], 1, v[34:35]
	v_lshl_add_u64 v[96:97], v[34:35], 0, v[78:79]
	global_load_dwordx4 v[66:69], v[96:97], off
	global_load_dwordx4 v[62:65], v[96:97], off offset:64
	global_load_dwordx4 v[58:61], v[96:97], off offset:128
	global_load_dwordx4 v[54:57], v[96:97], off offset:192
	v_add_u32_e32 v138, v87, v89
	s_movk_i32 s0, 0xff
	ds_read_b128 v[174:177], v138 offset:32768
	ds_read_b128 v[178:181], v138 offset:37120
	ds_read_b128 v[182:185], v138 offset:41472
	ds_read_b128 v[186:189], v138 offset:45824
	ds_read_b128 v[190:193], v138 offset:50176
	ds_read_b128 v[194:197], v138 offset:54528
	ds_read_b128 v[198:201], v138 offset:58880
	ds_read_b128 v[216:219], v138 offset:32832
	ds_read_b128 v[220:223], v138 offset:37184
	ds_read_b128 v[224:227], v138 offset:41536
	ds_read_b128 v[228:231], v138 offset:45888
	ds_read_b128 v[232:235], v138 offset:50240
	ds_read_b128 v[236:239], v138 offset:54592
	ds_read_b128 v[244:247], v138 offset:58944
	ds_read_b128 v[248:251], v138 offset:32896
	ds_read_b128 v[252:255], v138 offset:37248
	s_waitcnt vmcnt(3) lgkmcnt(15)
	v_mfma_f32_16x16x32_bf16 v[46:49], v[174:177], v[66:69], 0
	ds_read_b128 v[174:177], v138 offset:41600
	s_waitcnt lgkmcnt(15)
	v_mfma_f32_16x16x32_bf16 v[34:37], v[178:181], v[66:69], 0
	ds_read_b128 v[178:181], v138 offset:45952
	s_waitcnt lgkmcnt(15)
	v_mfma_f32_16x16x32_bf16 v[38:41], v[182:185], v[66:69], 0
	ds_read_b128 v[182:185], v138 offset:50304
	s_waitcnt lgkmcnt(15)
	v_mfma_f32_16x16x32_bf16 v[42:45], v[186:189], v[66:69], 0
	ds_read_b128 v[186:189], v138 offset:54656
	s_waitcnt lgkmcnt(15)
	v_mfma_f32_16x16x32_bf16 v[70:73], v[190:193], v[66:69], 0
	ds_read_b128 v[190:193], v138 offset:59008
	s_waitcnt lgkmcnt(15)
	v_mfma_f32_16x16x32_bf16 v[50:53], v[194:197], v[66:69], 0
	ds_read_b128 v[194:197], v138 offset:32960
	s_waitcnt lgkmcnt(15)
	v_mfma_f32_16x16x32_bf16 v[74:77], v[198:201], v[66:69], 0
	ds_read_b128 v[198:201], v138 offset:37312
	s_waitcnt vmcnt(2) lgkmcnt(15)
	v_mfma_f32_16x16x32_bf16 v[46:49], v[216:219], v[62:65], v[46:49]
	ds_read_b128 v[216:219], v138 offset:41664
	s_waitcnt lgkmcnt(15)
	v_mfma_f32_16x16x32_bf16 v[34:37], v[220:223], v[62:65], v[34:37]
	ds_read_b128 v[220:223], v138 offset:46016
	s_waitcnt lgkmcnt(15)
	v_mfma_f32_16x16x32_bf16 v[38:41], v[224:227], v[62:65], v[38:41]
	ds_read_b128 v[224:227], v138 offset:50368
	s_waitcnt lgkmcnt(15)
	v_mfma_f32_16x16x32_bf16 v[42:45], v[228:231], v[62:65], v[42:45]
	ds_read_b128 v[228:231], v138 offset:54720
	s_waitcnt lgkmcnt(15)
	v_mfma_f32_16x16x32_bf16 v[70:73], v[232:235], v[62:65], v[70:73]
	ds_read_b128 v[232:235], v138 offset:59072
	s_waitcnt lgkmcnt(15)
	v_mfma_f32_16x16x32_bf16 v[50:53], v[236:239], v[62:65], v[50:53]
	ds_read_b128 v[236:239], v138 offset:63232
	s_waitcnt lgkmcnt(15)
	v_mfma_f32_16x16x32_bf16 v[74:77], v[244:247], v[62:65], v[74:77]
	ds_read_b128 v[244:247], v138 offset:63296
	s_waitcnt vmcnt(1) lgkmcnt(15)
	v_mfma_f32_16x16x32_bf16 v[46:49], v[248:251], v[58:61], v[46:49]
	ds_read_b128 v[248:251], v138 offset:63360
	s_waitcnt lgkmcnt(15)
	v_mfma_f32_16x16x32_bf16 v[34:37], v[252:255], v[58:61], v[34:37]
	ds_read_b128 v[252:255], v138 offset:63424
	s_waitcnt lgkmcnt(15)
	v_mfma_f32_16x16x32_bf16 v[38:41], v[174:177], v[58:61], v[38:41]
	s_waitcnt lgkmcnt(14)
	v_mfma_f32_16x16x32_bf16 v[42:45], v[178:181], v[58:61], v[42:45]
	s_waitcnt lgkmcnt(13)
	v_mfma_f32_16x16x32_bf16 v[70:73], v[182:185], v[58:61], v[70:73]
	s_waitcnt lgkmcnt(12)
	v_mfma_f32_16x16x32_bf16 v[50:53], v[186:189], v[58:61], v[50:53]
	s_waitcnt lgkmcnt(11)
	v_mfma_f32_16x16x32_bf16 v[74:77], v[190:193], v[58:61], v[74:77]
	s_waitcnt vmcnt(0) lgkmcnt(10)
	v_mfma_f32_16x16x32_bf16 v[46:49], v[194:197], v[54:57], v[46:49]
	s_waitcnt lgkmcnt(9)
	v_mfma_f32_16x16x32_bf16 v[34:37], v[198:201], v[54:57], v[34:37]
	s_waitcnt lgkmcnt(8)
	v_mfma_f32_16x16x32_bf16 v[38:41], v[216:219], v[54:57], v[38:41]
	s_waitcnt lgkmcnt(7)
	v_mfma_f32_16x16x32_bf16 v[42:45], v[220:223], v[54:57], v[42:45]
	s_waitcnt lgkmcnt(6)
	v_mfma_f32_16x16x32_bf16 v[70:73], v[224:227], v[54:57], v[70:73]
	s_waitcnt lgkmcnt(5)
	v_mfma_f32_16x16x32_bf16 v[50:53], v[228:231], v[54:57], v[50:53]
	s_waitcnt lgkmcnt(4)
	v_mfma_f32_16x16x32_bf16 v[74:77], v[232:235], v[54:57], v[74:77]
	s_waitcnt lgkmcnt(3)
	v_mfma_f32_16x16x32_bf16 v[66:69], v[236:239], v[66:69], 0
	s_waitcnt lgkmcnt(2)
	v_mfma_f32_16x16x32_bf16 v[62:65], v[244:247], v[62:65], v[66:69]
	s_waitcnt lgkmcnt(1)
	v_mfma_f32_16x16x32_bf16 v[58:61], v[248:251], v[58:61], v[62:65]
	s_waitcnt lgkmcnt(0)
; #define LAS __attribute__((address_space(3)))
; __device__ __forceinline__ f32x4 mfma16(bf16x8 a, bf16x8 b, f32x4 c) { return __builtin_amdgcn_mfma_f32_16x16x32_bf16(a, b, c, 0, 0, 0); }
; __device__ __forceinline__ unsigned mono(float f) { const unsigned u = __float_as_uint(f); return (u & 0x80000000u) ? ~u : (u ^ 0x80000000u); }
; __device__ __forceinline__ void topk_phase(LAS unsigned char* lds, const bf16_t* qp, const bf16_t* keys, const float* SU, const float* SV, int* sel_e, float* sel_g, float* sel_su, int G, int b) {
;     ...
;                 for (int ks = 0; ks < 4; ++ks) { const bf16x8 a = *(const LAS bf16x8*)(kb + (mt * 16 + fr) * 136 + ks * 32 + fq * 8); acc[mt] = mfma16(a, bq[ks], acc[mt]); }
;             unsigned lo16[16];
; #pragma unroll
;             for (int mt = 0; mt < 4; ++mt)
; #pragma unroll
;                 for (int r = 0; r < 4; ++r) {
;                     T[p][mt * 4 + r] = (mono(acc[mt][r]) & ~127u) | (unsigned)(127 - (mt * 16 + fq * 4 + r));
;                     lo16[mt * 4 + r] = (mono(acc[mt + 4][r]) & ~127u) | (unsigned)(127 - ((mt + 4) * 16 + fq * 4 + r));
;                 }
;             SN_SORT16(T[p]); SN_SORT16(lo16);
	v_mfma_f32_16x16x32_bf16 v[54:57], v[252:255], v[54:57], v[58:61]
	s_nop 2
	v_ashrrev_i32_e32 v58, 31, v46
	v_bitop3_b32 v46, v46, v58, v132 bitop3:0x1e
	v_and_or_b32 v46, v46, s53, v98
	v_ashrrev_i32_e32 v58, 31, v70
	v_bitop3_b32 v58, v70, v58, v132 bitop3:0x1e
	v_and_or_b32 v58, v58, s53, v99
	v_ashrrev_i32_e32 v59, 31, v47
	v_bitop3_b32 v47, v47, v59, v132 bitop3:0x1e
	v_and_or_b32 v47, v47, s53, v100
	v_ashrrev_i32_e32 v59, 31, v71
	v_bitop3_b32 v59, v71, v59, v132 bitop3:0x1e
	v_and_or_b32 v59, v59, s53, v101
	v_ashrrev_i32_e32 v60, 31, v48
	v_bitop3_b32 v48, v48, v60, v132 bitop3:0x1e
	v_and_or_b32 v48, v48, s53, v102
	v_ashrrev_i32_e32 v60, 31, v72
	v_bitop3_b32 v60, v72, v60, v132 bitop3:0x1e
	v_and_or_b32 v60, v60, s53, v103
	v_ashrrev_i32_e32 v61, 31, v49
	v_bitop3_b32 v49, v49, v61, v132 bitop3:0x1e
	v_and_or_b32 v49, v49, s53, v104
	v_ashrrev_i32_e32 v61, 31, v73
	v_bitop3_b32 v61, v73, v61, v132 bitop3:0x1e
	v_and_or_b32 v61, v61, s53, v105
	v_ashrrev_i32_e32 v62, 31, v34
	v_bitop3_b32 v34, v34, v62, v132 bitop3:0x1e
	v_and_or_b32 v34, v34, s53, v106
	v_ashrrev_i32_e32 v62, 31, v50
	v_bitop3_b32 v50, v50, v62, v132 bitop3:0x1e
	v_and_or_b32 v50, v50, s53, v107
	v_ashrrev_i32_e32 v62, 31, v35
	v_bitop3_b32 v35, v35, v62, v132 bitop3:0x1e
	v_and_or_b32 v35, v35, s53, v108
	v_ashrrev_i32_e32 v62, 31, v51
	v_bitop3_b32 v51, v51, v62, v132 bitop3:0x1e
	v_and_or_b32 v51, v51, s53, v109
	v_ashrrev_i32_e32 v62, 31, v36
	v_bitop3_b32 v36, v36, v62, v132 bitop3:0x1e
	v_and_or_b32 v36, v36, s53, v110
	v_ashrrev_i32_e32 v62, 31, v52
	v_bitop3_b32 v52, v52, v62, v132 bitop3:0x1e
	v_and_or_b32 v52, v52, s53, v111
	v_ashrrev_i32_e32 v62, 31, v37
	v_bitop3_b32 v37, v37, v62, v132 bitop3:0x1e
	v_and_or_b32 v37, v37, s53, v112
	v_ashrrev_i32_e32 v62, 31, v53
	v_bitop3_b32 v53, v53, v62, v132 bitop3:0x1e
	v_and_or_b32 v53, v53, s53, v113
	v_ashrrev_i32_e32 v62, 31, v38
	v_bitop3_b32 v38, v38, v62, v132 bitop3:0x1e
	v_and_or_b32 v38, v38, s53, v114
	v_ashrrev_i32_e32 v62, 31, v74
	v_bitop3_b32 v62, v74, v62, v132 bitop3:0x1e
	v_max_u32_e32 v74, v58, v59
	v_ashrrev_i32_e32 v63, 31, v39
	v_cmp_lt_i32_e32 vcc, -1, v75
	v_bitop3_b32 v39, v39, v63, v132 bitop3:0x1e
	v_min_u32_e32 v58, v58, v59
	v_cndmask_b32_e32 v63, -1, v132, vcc
	v_max_u32_e32 v59, v60, v61
	v_min_u32_e32 v60, v60, v61
	v_ashrrev_i32_e32 v64, 31, v40
	v_cmp_lt_i32_e32 vcc, -1, v76
	v_bitop3_b32 v40, v40, v64, v132 bitop3:0x1e
	v_max_u32_e32 v61, v74, v59
	v_cndmask_b32_e32 v64, -1, v132, vcc
	v_min_u32_e32 v59, v74, v59
	v_max_u32_e32 v74, v58, v60
	v_ashrrev_i32_e32 v65, 31, v41
	v_cmp_lt_i32_e32 vcc, -1, v77
	v_bitop3_b32 v41, v41, v65, v132 bitop3:0x1e
	v_min_u32_e32 v58, v58, v60
	v_cndmask_b32_e32 v65, -1, v132, vcc
	v_max_u32_e32 v60, v74, v59
	v_min_u32_e32 v59, v74, v59
	v_ashrrev_i32_e32 v66, 31, v42
	v_bitop3_b32 v42, v42, v66, v132 bitop3:0x1e
	v_max_u32_e32 v74, v50, v51
	v_ashrrev_i32_e32 v66, 31, v54
	v_bitop3_b32 v54, v54, v66, v132 bitop3:0x1e
	v_min_u32_e32 v50, v50, v51
	v_ashrrev_i32_e32 v66, 31, v43
	v_bitop3_b32 v43, v43, v66, v132 bitop3:0x1e
	v_max_u32_e32 v51, v52, v53
	v_ashrrev_i32_e32 v66, 31, v55
	v_bitop3_b32 v55, v55, v66, v132 bitop3:0x1e
	v_min_u32_e32 v52, v52, v53
	v_ashrrev_i32_e32 v66, 31, v44
	v_bitop3_b32 v44, v44, v66, v132 bitop3:0x1e
	v_max_u32_e32 v53, v74, v51
	v_ashrrev_i32_e32 v66, 31, v56
	v_bitop3_b32 v56, v56, v66, v132 bitop3:0x1e
	v_min_u32_e32 v51, v74, v51
	v_ashrrev_i32_e32 v66, 31, v45
	v_cmp_lt_i32_e32 vcc, -1, v57
	v_bitop3_b32 v45, v45, v66, v132 bitop3:0x1e
	v_max_u32_e32 v74, v50, v52
	v_cndmask_b32_e32 v66, -1, v132, vcc
	v_xor_b32_e32 v57, v66, v57
	v_max_u32_e32 v66, v46, v47
	v_min_u32_e32 v46, v46, v47
	v_max_u32_e32 v47, v48, v49
	v_min_u32_e32 v48, v48, v49
	v_max_u32_e32 v49, v66, v47
	v_min_u32_e32 v47, v66, v47
	v_max_u32_e32 v66, v46, v48
	v_min_u32_e32 v46, v46, v48
	v_max_u32_e32 v48, v66, v47
	v_min_u32_e32 v47, v66, v47
	v_max_u32_e32 v66, v34, v35
	v_min_u32_e32 v34, v34, v35
	v_max_u32_e32 v35, v36, v37
	v_min_u32_e32 v36, v36, v37
	v_max_u32_e32 v37, v66, v35
	v_min_u32_e32 v35, v66, v35
	v_max_u32_e32 v66, v34, v36
	v_min_u32_e32 v34, v34, v36
	v_max_u32_e32 v36, v66, v35
	v_min_u32_e32 v35, v66, v35
	v_min_u32_e32 v50, v50, v52
	v_max_u32_e32 v52, v74, v51
	v_min_u32_e32 v51, v74, v51
	v_max_u32_e32 v66, v49, v37
	v_min_u32_e32 v37, v49, v37
	v_max_u32_e32 v49, v47, v35
	v_max_u32_e32 v74, v61, v53
	v_min_u32_e32 v53, v61, v53
	v_max_u32_e32 v61, v59, v51
	v_xor_b32_e32 v63, v63, v75
	v_xor_b32_e32 v64, v64, v76
	v_xor_b32_e32 v65, v65, v77
	v_min_u32_e32 v35, v47, v35
	v_max_u32_e32 v47, v49, v37
	v_min_u32_e32 v37, v49, v37
	v_max_u32_e32 v49, v48, v36
	v_min_u32_e32 v36, v48, v36
	v_max_u32_e32 v48, v46, v34
	v_min_u32_e32 v51, v59, v51
	v_max_u32_e32 v59, v61, v53
	v_min_u32_e32 v53, v61, v53
	v_max_u32_e32 v61, v60, v52
	v_min_u32_e32 v52, v60, v52
	v_max_u32_e32 v60, v58, v50
	v_and_or_b32 v62, v62, s53, v115
	v_and_or_b32 v39, v39, s53, v116
	v_and_or_b32 v63, v63, s53, v117
	v_and_or_b32 v40, v40, s53, v118
	v_and_or_b32 v64, v64, s53, v119
	v_and_or_b32 v41, v41, s53, v120
	v_and_or_b32 v65, v65, s53, v121
	v_min_u32_e32 v34, v46, v34
	v_max_u32_e32 v46, v48, v36
	v_min_u32_e32 v36, v48, v36
	v_min_u32_e32 v50, v58, v50
	v_max_u32_e32 v58, v60, v52
	v_min_u32_e32 v52, v60, v52
	v_max_u32_e32 v48, v49, v47
	v_min_u32_e32 v47, v49, v47
	v_max_u32_e32 v49, v46, v37
	v_min_u32_e32 v37, v46, v37
	v_max_u32_e32 v46, v36, v35
	v_min_u32_e32 v35, v36, v35
	v_max_u32_e32 v36, v38, v39
	v_min_u32_e32 v38, v38, v39
	v_max_u32_e32 v39, v40, v41
	v_min_u32_e32 v40, v40, v41
	v_max_u32_e32 v60, v61, v59
; __device__ __forceinline__ void topk_phase(LAS unsigned char* lds, const bf16_t* qp, const bf16_t* keys, const float* SU, const float* SV, int* sel_e, float* sel_g, float* sel_su, int G, int b) {
;     ...
;             SN_SORT16(T[p]); SN_SORT16(lo16);
; #pragma unroll
;             for (int i = 0; i < 16; ++i) T[p][i] = umax_(T[p][i], lo16[15 - i]);
;             SN_BITONIC16(T[p]);
	v_min_u32_e32 v59, v61, v59
	v_max_u32_e32 v61, v58, v53
	v_min_u32_e32 v53, v58, v53
	v_max_u32_e32 v58, v52, v51
	v_min_u32_e32 v51, v52, v51
	v_max_u32_e32 v52, v62, v63
	v_min_u32_e32 v62, v62, v63
	v_max_u32_e32 v63, v64, v65
	v_min_u32_e32 v64, v64, v65
	v_and_or_b32 v42, v42, s53, v122
	v_and_or_b32 v54, v54, s53, v123
	v_and_or_b32 v43, v43, s53, v124
	v_and_or_b32 v55, v55, s53, v125
	v_and_or_b32 v44, v44, s53, v126
	v_and_or_b32 v56, v56, s53, v127
	v_and_or_b32 v45, v45, s53, v128
	v_and_or_b32 v57, v57, s53, v129
	v_max_u32_e32 v41, v36, v39
	v_min_u32_e32 v36, v36, v39
	v_max_u32_e32 v39, v38, v40
	v_max_u32_e32 v65, v52, v63
	v_min_u32_e32 v52, v52, v63
	v_max_u32_e32 v63, v62, v64
	v_min_u32_e32 v38, v38, v40
	v_max_u32_e32 v40, v39, v36
	v_min_u32_e32 v36, v39, v36
	v_max_u32_e32 v39, v42, v43
	v_min_u32_e32 v42, v42, v43
	v_max_u32_e32 v43, v44, v45
	v_min_u32_e32 v44, v44, v45
	v_min_u32_e32 v62, v62, v64
	v_max_u32_e32 v64, v63, v52
	v_min_u32_e32 v52, v63, v52
	v_max_u32_e32 v63, v54, v55
	v_min_u32_e32 v54, v54, v55
	v_max_u32_e32 v55, v56, v57
	v_min_u32_e32 v56, v56, v57
	v_max_u32_e32 v45, v39, v43
	v_min_u32_e32 v39, v39, v43
	v_max_u32_e32 v43, v42, v44
	v_max_u32_e32 v57, v63, v55
	v_min_u32_e32 v55, v63, v55
	v_max_u32_e32 v63, v54, v56
	v_min_u32_e32 v42, v42, v44
	v_max_u32_e32 v44, v43, v39
	v_min_u32_e32 v39, v43, v39
	v_min_u32_e32 v54, v54, v56
	v_max_u32_e32 v56, v63, v55
	v_min_u32_e32 v55, v63, v55
	v_max_u32_e32 v43, v41, v45
	v_min_u32_e32 v41, v41, v45
	v_max_u32_e32 v45, v36, v39
	v_max_u32_e32 v63, v65, v57
	v_min_u32_e32 v57, v65, v57
	v_max_u32_e32 v65, v52, v55
	v_min_u32_e32 v36, v36, v39
	v_max_u32_e32 v39, v45, v41
	v_min_u32_e32 v41, v45, v41
	v_max_u32_e32 v45, v40, v44
	v_min_u32_e32 v40, v40, v44
	v_max_u32_e32 v44, v38, v42
	v_min_u32_e32 v52, v52, v55
	v_max_u32_e32 v55, v65, v57
	v_min_u32_e32 v57, v65, v57
	v_max_u32_e32 v65, v64, v56
	v_min_u32_e32 v56, v64, v56
	v_max_u32_e32 v64, v62, v54
	v_min_u32_e32 v38, v38, v42
	v_max_u32_e32 v42, v44, v40
	v_min_u32_e32 v54, v62, v54
	v_max_u32_e32 v62, v64, v56
	v_min_u32_e32 v40, v44, v40
	v_max_u32_e32 v44, v45, v39
	v_min_u32_e32 v39, v45, v39
	v_max_u32_e32 v45, v42, v41
	v_min_u32_e32 v41, v42, v41
	v_min_u32_e32 v56, v64, v56
	v_max_u32_e32 v64, v65, v55
	v_min_u32_e32 v55, v65, v55
	v_max_u32_e32 v65, v62, v57
	v_min_u32_e32 v57, v62, v57
	v_max_u32_e32 v42, v40, v36
	v_min_u32_e32 v36, v40, v36
	v_min_u32_e32 v40, v66, v43
	v_max_u32_e32 v67, v37, v41
	v_max_u32_e32 v62, v56, v52
	v_min_u32_e32 v52, v56, v52
	v_min_u32_e32 v56, v74, v63
	v_max_u32_e32 v75, v53, v57
	v_min_u32_e32 v37, v37, v41
	v_max_u32_e32 v41, v67, v40
	v_min_u32_e32 v40, v67, v40
	v_max_u32_e32 v67, v47, v39
	v_min_u32_e32 v39, v47, v39
	v_max_u32_e32 v47, v35, v36
	v_min_u32_e32 v53, v53, v57
	v_max_u32_e32 v57, v75, v56
	v_min_u32_e32 v56, v75, v56
	v_max_u32_e32 v75, v59, v55
	v_min_u32_e32 v55, v59, v55
	v_max_u32_e32 v59, v51, v52
	v_min_u32_e32 v35, v35, v36
	v_max_u32_e32 v36, v47, v39
	v_min_u32_e32 v39, v47, v39
	v_min_u32_e32 v51, v51, v52
	v_max_u32_e32 v52, v59, v55
	v_min_u32_e32 v55, v59, v55
	v_max_u32_e32 v47, v67, v41
	v_min_u32_e32 v41, v67, v41
	v_max_u32_e32 v67, v36, v40
	v_min_u32_e32 v36, v36, v40
	v_max_u32_e32 v40, v39, v37
	v_min_u32_e32 v37, v39, v37
	v_max_u32_e32 v39, v48, v44
	v_min_u32_e32 v44, v48, v44
	v_max_u32_e32 v48, v46, v42
	v_max_u32_e32 v59, v75, v57
	v_min_u32_e32 v57, v75, v57
	v_max_u32_e32 v75, v52, v56
	v_min_u32_e32 v52, v52, v56
	v_max_u32_e32 v56, v55, v53
	v_min_u32_e32 v53, v55, v53
	v_max_u32_e32 v55, v60, v64
	v_min_u32_e32 v60, v60, v64
	v_max_u32_e32 v64, v58, v62
	v_min_u32_e32 v42, v46, v42
	v_max_u32_e32 v46, v48, v44
	v_min_u32_e32 v44, v48, v44
	v_max_u32_e32 v48, v49, v45
	v_min_u32_e32 v45, v49, v45
	v_max_u32_e32 v49, v34, v38
	v_min_u32_e32 v58, v58, v62
	v_max_u32_e32 v62, v64, v60
	v_min_u32_e32 v60, v64, v60
	v_max_u32_e32 v64, v61, v65
	v_min_u32_e32 v61, v61, v65
	v_max_u32_e32 v65, v50, v54
	v_min_u32_e32 v34, v34, v38
	v_max_u32_e32 v38, v49, v45
	v_min_u32_e32 v45, v49, v45
	v_min_u32_e32 v50, v50, v54
	v_max_u32_e32 v54, v65, v61
	v_min_u32_e32 v61, v65, v61
	v_max_u32_e32 v49, v48, v46
	v_min_u32_e32 v46, v48, v46
	v_max_u32_e32 v48, v38, v44
	v_min_u32_e32 v38, v38, v44
	v_max_u32_e32 v44, v45, v42
	v_min_u32_e32 v42, v45, v42
	v_max_u32_e32 v65, v64, v62
	v_min_u32_e32 v62, v64, v62
	v_max_u32_e32 v64, v54, v60
	v_min_u32_e32 v54, v54, v60
	v_max_u32_e32 v60, v61, v58
	v_min_u32_e32 v58, v61, v58
	v_min_u32_e32 v45, v39, v47
	v_min_u32_e32 v68, v49, v41
	v_min_u32_e32 v69, v46, v67
	v_min_u32_e32 v70, v48, v36
	v_min_u32_e32 v71, v38, v40
	v_min_u32_e32 v72, v44, v37
	v_min_u32_e32 v73, v42, v35
	v_min_u32_e32 v61, v55, v59
	v_min_u32_e32 v76, v65, v57
	v_min_u32_e32 v77, v62, v75
	v_min_u32_e32 v134, v64, v52
	v_min_u32_e32 v135, v54, v56
	v_min_u32_e32 v136, v60, v53
	v_min_u32_e32 v137, v58, v51
	v_max3_u32 v43, v66, v43, v50
	v_max3_u32 v39, v39, v47, v137
	v_max3_u32 v45, v45, v58, v51
	v_max3_u32 v41, v49, v41, v136
	v_max3_u32 v47, v68, v60, v53
	v_max3_u32 v46, v46, v67, v135
	v_max3_u32 v49, v69, v54, v56
	v_max3_u32 v36, v48, v36, v134
	v_max3_u32 v48, v70, v64, v52
	v_max3_u32 v38, v38, v40, v77
	v_max3_u32 v40, v71, v62, v75
	v_max3_u32 v37, v44, v37, v76
	v_max3_u32 v44, v72, v65, v57
	v_max3_u32 v35, v42, v35, v61
	v_max3_u32 v42, v73, v55, v59
	v_max3_u32 v34, v34, v74, v63
	v_max_u32_e32 v50, v43, v48
	v_min_u32_e32 v43, v43, v48
	v_max_u32_e32 v48, v39, v38
	v_min_u32_e32 v38, v39, v38
	v_max_u32_e32 v39, v45, v40
	v_min_u32_e32 v40, v45, v40
	v_max_u32_e32 v45, v41, v37
; #define LAS __attribute__((address_space(3)))
; __device__ __forceinline__ f32x4 mfma16(bf16x8 a, bf16x8 b, f32x4 c) { return __builtin_amdgcn_mfma_f32_16x16x32_bf16(a, b, c, 0, 0, 0); }
; __device__ __forceinline__ void topk_phase(LAS unsigned char* lds, const bf16_t* qp, const bf16_t* keys, const float* SU, const float* SV, int* sel_e, float* sel_g, float* sel_su, int G, int b) {
;     ...
;         for (int p = 0; p < 2; ++p) {
;             f32x4 acc[8];
; #pragma unroll
;             for (int mt = 0; mt < 8; ++mt) acc[mt] = (f32x4){0.f, 0.f, 0.f, 0.f};
;             bf16x8 bq[4];
; #pragma unroll
;             for (int ks = 0; ks < 4; ++ks) bq[ks] = *(const bf16x8*)(qp + (size_t)tok * D_ + h * 256 + p * 128 + ks * 32 + fq * 8);
;             const LAS bf16_t* kb = KL + p * 128 * 136;
; #pragma unroll
;             for (int mt = 0; mt < 8; ++mt)
; #pragma unroll
;                 for (int ks = 0; ks < 4; ++ks) { const bf16x8 a = *(const LAS bf16x8*)(kb + (mt * 16 + fr) * 136 + ks * 32 + fq * 8); acc[mt] = mfma16(a, bq[ks], acc[mt]); }
;     ...
;             SN_BITONIC16(T[p]);
;             TOPK_XMERGE(T[p], 16); TOPK_XMERGE(T[p], 32);
	v_min_u32_e32 v37, v41, v37
	v_max_u32_e32 v41, v47, v44
	v_min_u32_e32 v44, v47, v44
	v_max_u32_e32 v47, v46, v35
	v_min_u32_e32 v35, v46, v35
	v_max_u32_e32 v46, v49, v42
	v_min_u32_e32 v42, v49, v42
	v_max_u32_e32 v49, v36, v34
	v_min_u32_e32 v34, v36, v34
	v_max_u32_e32 v36, v50, v41
	v_min_u32_e32 v41, v50, v41
	v_max_u32_e32 v50, v48, v47
	v_min_u32_e32 v47, v48, v47
	v_max_u32_e32 v48, v39, v46
	v_min_u32_e32 v39, v39, v46
	v_max_u32_e32 v46, v45, v49
	v_min_u32_e32 v45, v45, v49
	v_max_u32_e32 v49, v43, v44
	v_min_u32_e32 v43, v43, v44
	v_max_u32_e32 v44, v38, v35
	v_min_u32_e32 v35, v38, v35
	v_max_u32_e32 v38, v40, v42
	v_min_u32_e32 v40, v40, v42
	v_max_u32_e32 v42, v37, v34
	v_min_u32_e32 v34, v37, v34
	v_max_u32_e32 v37, v36, v48
	v_min_u32_e32 v36, v36, v48
	v_max_u32_e32 v48, v50, v46
	v_min_u32_e32 v46, v50, v46
	v_max_u32_e32 v50, v41, v39
	v_min_u32_e32 v39, v41, v39
	v_max_u32_e32 v41, v47, v45
	v_min_u32_e32 v45, v47, v45
	v_max_u32_e32 v47, v49, v38
	v_min_u32_e32 v38, v49, v38
	v_max_u32_e32 v49, v44, v42
	v_min_u32_e32 v42, v44, v42
	v_max_u32_e32 v44, v43, v40
	v_min_u32_e32 v40, v43, v40
	v_max_u32_e32 v43, v35, v34
	v_min_u32_e32 v34, v35, v34
	v_max_u32_e32 v35, v37, v48
	v_min_u32_e32 v37, v37, v48
	v_max_u32_e32 v48, v36, v46
	v_min_u32_e32 v36, v36, v46
	v_max_u32_e32 v46, v50, v41
	v_min_u32_e32 v41, v50, v41
	v_max_u32_e32 v50, v39, v45
	v_min_u32_e32 v39, v39, v45
	v_max_u32_e32 v45, v47, v49
	v_min_u32_e32 v47, v47, v49
	v_max_u32_e32 v49, v38, v42
	v_min_u32_e32 v38, v38, v42
	v_max_u32_e32 v42, v44, v43
	v_min_u32_e32 v43, v44, v43
	v_max_u32_e32 v44, v40, v34
	v_min_u32_e32 v34, v40, v34
	v_mov_b32_e32 v40, v35
	v_mov_b32_e32 v51, v37
	v_mov_b32_e32 v52, v48
	v_mov_b32_e32 v53, v36
	v_mov_b32_e32 v54, v46
	v_mov_b32_e32 v55, v41
	v_mov_b32_e32 v56, v50
	v_mov_b32_e32 v57, v39
	v_mov_b32_e32 v58, v45
	v_mov_b32_e32 v59, v47
	v_mov_b32_e32 v60, v49
	v_mov_b32_e32 v61, v38
	v_mov_b32_e32 v62, v42
	v_mov_b32_e32 v63, v43
	v_mov_b32_e32 v64, v44
	v_mov_b32_e32 v65, v34
	v_permlane16_swap_b32_e32 v35, v40
	v_permlane16_swap_b32_e32 v37, v51
	v_permlane16_swap_b32_e32 v48, v52
	v_permlane16_swap_b32_e32 v36, v53
	v_permlane16_swap_b32_e32 v46, v54
	v_permlane16_swap_b32_e32 v41, v55
	v_permlane16_swap_b32_e32 v50, v56
	v_permlane16_swap_b32_e32 v39, v57
	v_permlane16_swap_b32_e32 v45, v58
	v_permlane16_swap_b32_e32 v47, v59
	v_permlane16_swap_b32_e32 v49, v60
	v_permlane16_swap_b32_e32 v38, v61
	v_permlane16_swap_b32_e32 v42, v62
	v_permlane16_swap_b32_e32 v43, v63
	v_permlane16_swap_b32_e32 v44, v64
	v_permlane16_swap_b32_e32 v34, v65
	v_max_u32_e32 v35, v35, v65
	v_max_u32_e32 v37, v37, v64
	v_max_u32_e32 v48, v48, v63
	v_max_u32_e32 v36, v36, v62
	v_max_u32_e32 v46, v46, v61
	v_max_u32_e32 v41, v41, v60
	v_max_u32_e32 v50, v50, v59
	v_max_u32_e32 v39, v39, v58
	v_max_u32_e32 v45, v45, v57
	v_max_u32_e32 v47, v47, v56
	v_max_u32_e32 v49, v49, v55
	v_max_u32_e32 v38, v38, v54
	v_max_u32_e32 v42, v42, v53
	v_max_u32_e32 v43, v43, v52
	v_max_u32_e32 v44, v44, v51
	v_max_u32_e32 v34, v34, v40
	v_max_u32_e32 v40, v35, v45
	v_min_u32_e32 v35, v35, v45
	v_max_u32_e32 v45, v37, v47
	v_min_u32_e32 v37, v37, v47
	v_max_u32_e32 v47, v48, v49
	v_min_u32_e32 v48, v48, v49
	v_max_u32_e32 v49, v36, v38
	v_min_u32_e32 v36, v36, v38
	v_max_u32_e32 v38, v46, v42
	v_min_u32_e32 v42, v46, v42
	v_max_u32_e32 v46, v41, v43
	v_min_u32_e32 v41, v41, v43
	v_max_u32_e32 v43, v50, v44
	v_min_u32_e32 v44, v50, v44
	v_max_u32_e32 v50, v39, v34
	v_min_u32_e32 v34, v39, v34
	v_max_u32_e32 v39, v40, v38
	v_min_u32_e32 v38, v40, v38
	v_max_u32_e32 v40, v45, v46
	v_min_u32_e32 v45, v45, v46
	v_max_u32_e32 v46, v47, v43
	v_min_u32_e32 v43, v47, v43
	v_max_u32_e32 v47, v49, v50
	v_min_u32_e32 v49, v49, v50
	v_max_u32_e32 v50, v35, v42
	v_min_u32_e32 v35, v35, v42
	v_max_u32_e32 v42, v37, v41
	v_min_u32_e32 v37, v37, v41
	v_max_u32_e32 v41, v48, v44
	v_min_u32_e32 v44, v48, v44
	v_max_u32_e32 v48, v36, v34
	v_min_u32_e32 v34, v36, v34
	v_max_u32_e32 v36, v39, v46
	v_min_u32_e32 v39, v39, v46
	v_max_u32_e32 v46, v40, v47
	v_min_u32_e32 v40, v40, v47
	v_max_u32_e32 v47, v38, v43
	v_min_u32_e32 v38, v38, v43
	v_max_u32_e32 v43, v45, v49
	v_min_u32_e32 v45, v45, v49
	v_max_u32_e32 v49, v50, v41
	v_min_u32_e32 v41, v50, v41
	v_max_u32_e32 v50, v42, v48
	v_min_u32_e32 v42, v42, v48
	v_max_u32_e32 v48, v35, v44
	v_min_u32_e32 v35, v35, v44
	v_max_u32_e32 v44, v37, v34
	v_min_u32_e32 v34, v37, v34
	v_max_u32_e32 v70, v36, v46
	v_min_u32_e32 v71, v36, v46
	v_max_u32_e32 v72, v39, v40
	v_min_u32_e32 v73, v39, v40
	v_max_u32_e32 v74, v47, v43
	v_min_u32_e32 v75, v47, v43
	v_max_u32_e32 v76, v38, v45
	v_min_u32_e32 v77, v38, v45
	v_max_u32_e32 v134, v49, v50
	v_min_u32_e32 v135, v49, v50
	v_max_u32_e32 v136, v41, v42
	v_min_u32_e32 v137, v41, v42
	v_max_u32_e32 v138, v48, v44
	v_min_u32_e32 v139, v48, v44
	v_max_u32_e32 v140, v35, v34
	v_min_u32_e32 v141, v35, v34
	global_load_dwordx4 v[46:49], v[96:97], off offset:256
	global_load_dwordx4 v[42:45], v[96:97], off offset:320
	global_load_dwordx4 v[38:41], v[96:97], off offset:384
	global_load_dwordx4 v[34:37], v[96:97], off offset:448
	ds_read_b128 v[50:53], v131 offset:34816
	ds_read_b128 v[54:57], v131 offset:34880
	s_waitcnt vmcnt(3) lgkmcnt(1)
	v_mfma_f32_16x16x32_bf16 v[50:53], v[50:53], v[46:49], 0
	ds_read_b128 v[58:61], v131 offset:39232
	ds_read_b128 v[62:65], v131 offset:43584
	ds_read_b128 v[66:69], v131 offset:47936
	s_waitcnt vmcnt(2) lgkmcnt(3)
	v_mfma_f32_16x16x32_bf16 v[50:53], v[54:57], v[42:45], v[50:53]
	ds_read_b128 v[54:57], v131 offset:34944
	ds_read_b128 v[158:161], v131 offset:52288
	ds_read_b128 v[162:165], v131 offset:56640
	s_waitcnt vmcnt(1) lgkmcnt(2)
; #define LAS __attribute__((address_space(3)))
; __device__ __forceinline__ f32x4 mfma16(bf16x8 a, bf16x8 b, f32x4 c) { return __builtin_amdgcn_mfma_f32_16x16x32_bf16(a, b, c, 0, 0, 0); }
; __device__ __forceinline__ void topk_phase(LAS unsigned char* lds, const bf16_t* qp, const bf16_t* keys, const float* SU, const float* SV, int* sel_e, float* sel_g, float* sel_su, int G, int b) {
;     ...
;             for (int ks = 0; ks < 4; ++ks) bq[ks] = *(const bf16x8*)(qp + (size_t)tok * D_ + h * 256 + p * 128 + ks * 32 + fq * 8);
;             const LAS bf16_t* kb = KL + p * 128 * 136;
; #pragma unroll
;             for (int mt = 0; mt < 8; ++mt)
; #pragma unroll
;                 for (int ks = 0; ks < 4; ++ks) { const bf16x8 a = *(const LAS bf16x8*)(kb + (mt * 16 + fr) * 136 + ks * 32 + fq * 8); acc[mt] = mfma16(a, bq[ks], acc[mt]); }
	v_mfma_f32_16x16x32_bf16 v[50:53], v[54:57], v[38:41], v[50:53]
	ds_read_b128 v[54:57], v131 offset:35008
	ds_read_b128 v[166:169], v131 offset:60992
	v_mov_b32_e32 v142, v70
	s_waitcnt vmcnt(0) lgkmcnt(1)
	v_mfma_f32_16x16x32_bf16 v[50:53], v[54:57], v[34:37], v[50:53]
	ds_read_b128 v[54:57], v131 offset:39168
	v_mov_b32_e32 v143, v71
	v_mov_b32_e32 v144, v72
	s_waitcnt lgkmcnt(0)
	v_mfma_f32_16x16x32_bf16 v[54:57], v[54:57], v[46:49], 0
	s_nop 2
	v_mov_b32_e32 v145, v73
	v_mov_b32_e32 v146, v74
	v_mfma_f32_16x16x32_bf16 v[54:57], v[58:61], v[42:45], v[54:57]
	ds_read_b128 v[58:61], v131 offset:39296
	v_mov_b32_e32 v147, v75
	v_mov_b32_e32 v148, v76
	s_waitcnt lgkmcnt(0)
	v_mfma_f32_16x16x32_bf16 v[54:57], v[58:61], v[38:41], v[54:57]
	ds_read_b128 v[58:61], v131 offset:39360
	v_mov_b32_e32 v149, v77
	v_mov_b32_e32 v150, v134
	s_waitcnt lgkmcnt(0)
	v_mfma_f32_16x16x32_bf16 v[54:57], v[58:61], v[34:37], v[54:57]
	ds_read_b128 v[58:61], v131 offset:43520
	v_mov_b32_e32 v151, v135
	v_mov_b32_e32 v152, v136
	s_waitcnt lgkmcnt(0)
	v_mfma_f32_16x16x32_bf16 v[58:61], v[58:61], v[46:49], 0
	v_mov_b32_e32 v153, v137
	v_mov_b32_e32 v154, v138
	v_mov_b32_e32 v155, v139
	v_mfma_f32_16x16x32_bf16 v[58:61], v[62:65], v[42:45], v[58:61]
	ds_read_b128 v[62:65], v131 offset:43648
	v_mov_b32_e32 v156, v140
	v_mov_b32_e32 v157, v141
	s_waitcnt lgkmcnt(0)
	v_mfma_f32_16x16x32_bf16 v[58:61], v[62:65], v[38:41], v[58:61]
	ds_read_b128 v[62:65], v131 offset:43712
	v_permlane32_swap_b32_e32 v70, v142
	s_waitcnt lgkmcnt(0)
	v_mfma_f32_16x16x32_bf16 v[58:61], v[62:65], v[34:37], v[58:61]
	ds_read_b128 v[62:65], v131 offset:47872
	v_permlane32_swap_b32_e32 v71, v143
	s_waitcnt lgkmcnt(0)
	v_mfma_f32_16x16x32_bf16 v[62:65], v[62:65], v[46:49], 0
	v_permlane32_swap_b32_e32 v72, v144
	v_permlane32_swap_b32_e32 v73, v145
	v_mfma_f32_16x16x32_bf16 v[62:65], v[66:69], v[42:45], v[62:65]
	ds_read_b128 v[66:69], v131 offset:48000
	v_permlane32_swap_b32_e32 v74, v146
	s_waitcnt lgkmcnt(0)
	v_mfma_f32_16x16x32_bf16 v[62:65], v[66:69], v[38:41], v[62:65]
	ds_read_b128 v[66:69], v131 offset:48064
	v_permlane32_swap_b32_e32 v75, v147
	s_waitcnt lgkmcnt(0)
	v_mfma_f32_16x16x32_bf16 v[62:65], v[66:69], v[34:37], v[62:65]
	ds_read_b128 v[66:69], v131 offset:52224
	v_permlane32_swap_b32_e32 v76, v148
	s_waitcnt lgkmcnt(0)
	v_mfma_f32_16x16x32_bf16 v[66:69], v[66:69], v[46:49], 0
	v_permlane32_swap_b32_e32 v77, v149
	v_permlane32_swap_b32_e32 v134, v150
	v_mfma_f32_16x16x32_bf16 v[66:69], v[158:161], v[42:45], v[66:69]
	ds_read_b128 v[158:161], v131 offset:52352
	v_permlane32_swap_b32_e32 v135, v151
	s_waitcnt lgkmcnt(0)
	v_mfma_f32_16x16x32_bf16 v[66:69], v[158:161], v[38:41], v[66:69]
	ds_read_b128 v[158:161], v131 offset:52416
	v_permlane32_swap_b32_e32 v136, v152
	s_waitcnt lgkmcnt(0)
	v_mfma_f32_16x16x32_bf16 v[66:69], v[158:161], v[34:37], v[66:69]
	ds_read_b128 v[158:161], v131 offset:56576
	v_permlane32_swap_b32_e32 v137, v153
	s_waitcnt lgkmcnt(0)
	v_mfma_f32_16x16x32_bf16 v[158:161], v[158:161], v[46:49], 0
	v_permlane32_swap_b32_e32 v138, v154
	v_permlane32_swap_b32_e32 v139, v155
	v_mfma_f32_16x16x32_bf16 v[158:161], v[162:165], v[42:45], v[158:161]
	ds_read_b128 v[162:165], v131 offset:56704
	v_permlane32_swap_b32_e32 v140, v156
	s_waitcnt lgkmcnt(0)
	v_mfma_f32_16x16x32_bf16 v[158:161], v[162:165], v[38:41], v[158:161]
	ds_read_b128 v[162:165], v131 offset:56768
	v_permlane32_swap_b32_e32 v141, v157
	s_waitcnt lgkmcnt(0)
	v_mfma_f32_16x16x32_bf16 v[158:161], v[162:165], v[34:37], v[158:161]
	ds_read_b128 v[162:165], v131 offset:60928
	s_waitcnt lgkmcnt(0)
	v_mfma_f32_16x16x32_bf16 v[162:165], v[162:165], v[46:49], 0
	v_mfma_f32_16x16x32_bf16 v[162:165], v[166:169], v[42:45], v[162:165]
	ds_read_b128 v[166:169], v131 offset:61056
	s_waitcnt lgkmcnt(0)
	v_mfma_f32_16x16x32_bf16 v[162:165], v[166:169], v[38:41], v[162:165]
	ds_read_b128 v[166:169], v131 offset:61120
	s_waitcnt lgkmcnt(0)
	v_mfma_f32_16x16x32_bf16 v[162:165], v[166:169], v[34:37], v[162:165]
	ds_read_b128 v[166:169], v131 offset:65280
	s_waitcnt lgkmcnt(0)
	v_mfma_f32_16x16x32_bf16 v[46:49], v[166:169], v[46:49], 0
	ds_read_b128 v[166:169], v131 offset:65344
	s_waitcnt lgkmcnt(0)
	v_mfma_f32_16x16x32_bf16 v[42:45], v[166:169], v[42:45], v[46:49]
	s_nop 4
	ds_read_b128 v[46:49], v131 offset:65408
	s_waitcnt lgkmcnt(0)
	v_mfma_f32_16x16x32_bf16 v[38:41], v[46:49], v[38:41], v[42:45]
	s_nop 2
	ds_read_b128 v[42:45], v131 offset:65472
	s_waitcnt lgkmcnt(0)
; __device__ __forceinline__ unsigned mono(float f) { const unsigned u = __float_as_uint(f); return (u & 0x80000000u) ? ~u : (u ^ 0x80000000u); }
; __device__ __forceinline__ void topk_phase(LAS unsigned char* lds, const bf16_t* qp, const bf16_t* keys, const float* SU, const float* SV, int* sel_e, float* sel_g, float* sel_su, int G, int b) {
;     ...
;             unsigned lo16[16];
; #pragma unroll
;             for (int mt = 0; mt < 4; ++mt)
; #pragma unroll
;                 for (int r = 0; r < 4; ++r) {
;                     T[p][mt * 4 + r] = (mono(acc[mt][r]) & ~127u) | (unsigned)(127 - (mt * 16 + fq * 4 + r));
;                     lo16[mt * 4 + r] = (mono(acc[mt + 4][r]) & ~127u) | (unsigned)(127 - ((mt + 4) * 16 + fq * 4 + r));
;                 }
;             SN_SORT16(T[p]); SN_SORT16(lo16);
	v_mfma_f32_16x16x32_bf16 v[34:37], v[42:45], v[34:37], v[38:41]
	s_nop 2
	v_ashrrev_i32_e32 v38, 31, v50
	v_bitop3_b32 v38, v50, v38, v132 bitop3:0x1e
	v_and_or_b32 v38, v38, s53, v98
	v_ashrrev_i32_e32 v39, 31, v66
	v_bitop3_b32 v39, v66, v39, v132 bitop3:0x1e
	v_and_or_b32 v39, v39, s53, v99
	v_ashrrev_i32_e32 v40, 31, v51
	v_bitop3_b32 v40, v51, v40, v132 bitop3:0x1e
	v_and_or_b32 v40, v40, s53, v100
	v_ashrrev_i32_e32 v41, 31, v67
	v_bitop3_b32 v41, v67, v41, v132 bitop3:0x1e
	v_and_or_b32 v41, v41, s53, v101
	v_ashrrev_i32_e32 v42, 31, v52
	v_bitop3_b32 v42, v52, v42, v132 bitop3:0x1e
	v_and_or_b32 v42, v42, s53, v102
	v_ashrrev_i32_e32 v43, 31, v68
	v_bitop3_b32 v43, v68, v43, v132 bitop3:0x1e
	v_and_or_b32 v43, v43, s53, v103
	v_ashrrev_i32_e32 v44, 31, v53
	v_bitop3_b32 v44, v53, v44, v132 bitop3:0x1e
	v_and_or_b32 v44, v44, s53, v104
	v_ashrrev_i32_e32 v45, 31, v69
	v_bitop3_b32 v45, v69, v45, v132 bitop3:0x1e
	v_and_or_b32 v45, v45, s53, v105
	v_ashrrev_i32_e32 v46, 31, v54
	v_bitop3_b32 v46, v54, v46, v132 bitop3:0x1e
	v_and_or_b32 v46, v46, s53, v106
	v_ashrrev_i32_e32 v47, 31, v158
	v_bitop3_b32 v47, v158, v47, v132 bitop3:0x1e
	v_and_or_b32 v47, v47, s53, v107
	v_ashrrev_i32_e32 v48, 31, v55
	v_bitop3_b32 v48, v55, v48, v132 bitop3:0x1e
	v_and_or_b32 v48, v48, s53, v108
	v_ashrrev_i32_e32 v49, 31, v159
	v_bitop3_b32 v49, v159, v49, v132 bitop3:0x1e
	v_and_or_b32 v49, v49, s53, v109
	v_ashrrev_i32_e32 v50, 31, v56
	v_bitop3_b32 v50, v56, v50, v132 bitop3:0x1e
	v_and_or_b32 v50, v50, s53, v110
	v_ashrrev_i32_e32 v51, 31, v160
	v_bitop3_b32 v51, v160, v51, v132 bitop3:0x1e
	v_max_u32_e32 v160, v39, v41
	v_ashrrev_i32_e32 v52, 31, v57
	v_bitop3_b32 v52, v57, v52, v132 bitop3:0x1e
	v_min_u32_e32 v39, v39, v41
	v_ashrrev_i32_e32 v53, 31, v161
	v_bitop3_b32 v53, v161, v53, v132 bitop3:0x1e
	v_max_u32_e32 v41, v43, v45
	v_ashrrev_i32_e32 v54, 31, v58
	v_cmp_lt_i32_e32 vcc, -1, v162
	v_bitop3_b32 v54, v58, v54, v132 bitop3:0x1e
	v_min_u32_e32 v43, v43, v45
	v_cndmask_b32_e32 v55, -1, v132, vcc
	v_and_or_b32 v51, v51, s53, v111
	v_and_or_b32 v52, v52, s53, v112
	v_ashrrev_i32_e32 v56, 31, v59
	v_cmp_lt_i32_e32 vcc, -1, v163
	v_bitop3_b32 v56, v59, v56, v132 bitop3:0x1e
	v_and_or_b32 v53, v53, s53, v113
	v_cndmask_b32_e32 v57, -1, v132, vcc
	v_max_u32_e32 v45, v160, v41
	v_min_u32_e32 v41, v160, v41
	v_ashrrev_i32_e32 v58, 31, v60
	v_cmp_lt_i32_e32 vcc, -1, v164
	v_bitop3_b32 v58, v60, v58, v132 bitop3:0x1e
	v_max_u32_e32 v160, v39, v43
	v_cndmask_b32_e32 v59, -1, v132, vcc
	v_min_u32_e32 v39, v39, v43
	v_max_u32_e32 v43, v160, v41
	v_ashrrev_i32_e32 v60, 31, v61
	v_cmp_lt_i32_e32 vcc, -1, v165
	v_bitop3_b32 v60, v61, v60, v132 bitop3:0x1e
	v_min_u32_e32 v41, v160, v41
	v_cndmask_b32_e32 v61, -1, v132, vcc
	v_max_u32_e32 v160, v47, v49
	v_min_u32_e32 v47, v47, v49
	v_ashrrev_i32_e32 v66, 31, v62
	v_bitop3_b32 v62, v62, v66, v132 bitop3:0x1e
	v_max_u32_e32 v49, v51, v53
	v_ashrrev_i32_e32 v66, 31, v34
	v_bitop3_b32 v34, v34, v66, v132 bitop3:0x1e
	v_min_u32_e32 v51, v51, v53
	v_ashrrev_i32_e32 v66, 31, v63
	v_bitop3_b32 v63, v63, v66, v132 bitop3:0x1e
	v_max_u32_e32 v53, v160, v49
	v_ashrrev_i32_e32 v66, 31, v35
	v_bitop3_b32 v35, v35, v66, v132 bitop3:0x1e
	v_min_u32_e32 v49, v160, v49
	v_ashrrev_i32_e32 v66, 31, v64
	v_bitop3_b32 v64, v64, v66, v132 bitop3:0x1e
	v_max_u32_e32 v160, v47, v51
	v_ashrrev_i32_e32 v66, 31, v36
	v_bitop3_b32 v36, v36, v66, v132 bitop3:0x1e
	v_min_u32_e32 v47, v47, v51
	v_ashrrev_i32_e32 v66, 31, v65
	v_cmp_lt_i32_e32 vcc, -1, v37
	v_bitop3_b32 v65, v65, v66, v132 bitop3:0x1e
	v_max_u32_e32 v51, v160, v49
	v_cndmask_b32_e32 v66, -1, v132, vcc
	v_xor_b32_e32 v37, v66, v37
	v_max_u32_e32 v66, v38, v40
	v_min_u32_e32 v38, v38, v40
	v_max_u32_e32 v40, v42, v44
	v_min_u32_e32 v42, v42, v44
	v_max_u32_e32 v44, v66, v40
	v_min_u32_e32 v40, v66, v40
	v_max_u32_e32 v66, v38, v42
	v_min_u32_e32 v38, v38, v42
	v_max_u32_e32 v42, v66, v40
	v_min_u32_e32 v40, v66, v40
	v_max_u32_e32 v66, v46, v48
	v_min_u32_e32 v46, v46, v48
	v_max_u32_e32 v48, v50, v52
	v_min_u32_e32 v50, v50, v52
	v_max_u32_e32 v52, v66, v48
	v_min_u32_e32 v48, v66, v48
	v_max_u32_e32 v66, v46, v50
	v_min_u32_e32 v46, v46, v50
	v_max_u32_e32 v50, v66, v48
	v_min_u32_e32 v48, v66, v48
	v_min_u32_e32 v49, v160, v49
	v_max_u32_e32 v66, v44, v52
	v_min_u32_e32 v44, v44, v52
	v_max_u32_e32 v52, v40, v48
	v_max_u32_e32 v160, v45, v53
	v_min_u32_e32 v45, v45, v53
	v_max_u32_e32 v53, v41, v49
	v_xor_b32_e32 v55, v55, v162
	v_xor_b32_e32 v57, v57, v163
	v_xor_b32_e32 v59, v59, v164
	v_xor_b32_e32 v61, v61, v165
	v_min_u32_e32 v40, v40, v48
	v_max_u32_e32 v48, v52, v44
	v_min_u32_e32 v44, v52, v44
	v_max_u32_e32 v52, v42, v50
	v_min_u32_e32 v42, v42, v50
	v_max_u32_e32 v50, v38, v46
	v_min_u32_e32 v41, v41, v49
	v_max_u32_e32 v49, v53, v45
	v_min_u32_e32 v45, v53, v45
	v_max_u32_e32 v53, v43, v51
	v_min_u32_e32 v43, v43, v51
	v_max_u32_e32 v51, v39, v47
	v_and_or_b32 v54, v54, s53, v114
	v_and_or_b32 v55, v55, s53, v115
	v_and_or_b32 v56, v56, s53, v116
	v_and_or_b32 v57, v57, s53, v117
	v_and_or_b32 v58, v58, s53, v118
	v_and_or_b32 v59, v59, s53, v119
	v_and_or_b32 v60, v60, s53, v120
	v_and_or_b32 v61, v61, s53, v121
	v_min_u32_e32 v38, v38, v46
	v_max_u32_e32 v46, v50, v42
	v_min_u32_e32 v42, v50, v42
	v_min_u32_e32 v39, v39, v47
	v_max_u32_e32 v47, v51, v43
	v_min_u32_e32 v43, v51, v43
	v_max_u32_e32 v50, v52, v48
	v_min_u32_e32 v48, v52, v48
	v_max_u32_e32 v52, v46, v44
	v_min_u32_e32 v44, v46, v44
	v_max_u32_e32 v46, v42, v40
	v_min_u32_e32 v40, v42, v40
	v_max_u32_e32 v42, v54, v56
	v_min_u32_e32 v54, v54, v56
	v_max_u32_e32 v56, v58, v60
; __device__ __forceinline__ void topk_phase(LAS unsigned char* lds, const bf16_t* qp, const bf16_t* keys, const float* SU, const float* SV, int* sel_e, float* sel_g, float* sel_su, int G, int b) {
;     ...
;             SN_SORT16(T[p]); SN_SORT16(lo16);
; #pragma unroll
;             for (int i = 0; i < 16; ++i) T[p][i] = umax_(T[p][i], lo16[15 - i]);
;             SN_BITONIC16(T[p]);
	v_min_u32_e32 v58, v58, v60
	v_max_u32_e32 v51, v53, v49
	v_min_u32_e32 v49, v53, v49
	v_max_u32_e32 v53, v47, v45
	v_min_u32_e32 v45, v47, v45
	v_max_u32_e32 v47, v43, v41
	v_min_u32_e32 v41, v43, v41
	v_max_u32_e32 v43, v55, v57
	v_min_u32_e32 v55, v55, v57
	v_max_u32_e32 v57, v59, v61
	v_min_u32_e32 v59, v59, v61
	v_and_or_b32 v62, v62, s53, v122
	v_and_or_b32 v34, v34, s53, v123
	v_and_or_b32 v63, v63, s53, v124
	v_and_or_b32 v35, v35, s53, v125
	v_and_or_b32 v64, v64, s53, v126
	v_and_or_b32 v36, v36, s53, v127
	v_and_or_b32 v65, v65, s53, v128
	v_and_or_b32 v37, v37, s53, v129
	v_max_u32_e32 v60, v42, v56
	v_min_u32_e32 v42, v42, v56
	v_max_u32_e32 v56, v54, v58
	v_max_u32_e32 v61, v43, v57
	v_min_u32_e32 v43, v43, v57
	v_max_u32_e32 v57, v55, v59
	v_min_u32_e32 v54, v54, v58
	v_max_u32_e32 v58, v56, v42
	v_min_u32_e32 v42, v56, v42
	v_max_u32_e32 v56, v62, v63
	v_min_u32_e32 v62, v62, v63
	v_max_u32_e32 v63, v64, v65
	v_min_u32_e32 v64, v64, v65
	v_min_u32_e32 v55, v55, v59
	v_max_u32_e32 v59, v57, v43
	v_min_u32_e32 v43, v57, v43
	v_max_u32_e32 v57, v34, v35
	v_min_u32_e32 v34, v34, v35
	v_max_u32_e32 v35, v36, v37
	v_min_u32_e32 v36, v36, v37
	v_max_u32_e32 v65, v56, v63
	v_min_u32_e32 v56, v56, v63
	v_max_u32_e32 v63, v62, v64
	v_max_u32_e32 v37, v57, v35
	v_min_u32_e32 v35, v57, v35
	v_max_u32_e32 v57, v34, v36
	v_min_u32_e32 v62, v62, v64
	v_max_u32_e32 v64, v63, v56
	v_min_u32_e32 v56, v63, v56
	v_min_u32_e32 v34, v34, v36
	v_max_u32_e32 v36, v57, v35
	v_min_u32_e32 v35, v57, v35
	v_max_u32_e32 v63, v60, v65
	v_min_u32_e32 v60, v60, v65
	v_max_u32_e32 v65, v42, v56
	v_max_u32_e32 v57, v61, v37
	v_min_u32_e32 v37, v61, v37
	v_max_u32_e32 v61, v43, v35
	v_min_u32_e32 v42, v42, v56
	v_max_u32_e32 v56, v65, v60
	v_min_u32_e32 v60, v65, v60
	v_max_u32_e32 v65, v58, v64
	v_min_u32_e32 v58, v58, v64
	v_max_u32_e32 v64, v54, v62
	v_min_u32_e32 v35, v43, v35
	v_max_u32_e32 v43, v61, v37
	v_min_u32_e32 v37, v61, v37
	v_max_u32_e32 v61, v59, v36
	v_min_u32_e32 v36, v59, v36
	v_max_u32_e32 v59, v55, v34
	v_min_u32_e32 v54, v54, v62
	v_max_u32_e32 v62, v64, v58
	v_min_u32_e32 v34, v55, v34
	v_max_u32_e32 v55, v59, v36
	v_min_u32_e32 v58, v64, v58
	v_max_u32_e32 v64, v65, v56
	v_min_u32_e32 v56, v65, v56
	v_max_u32_e32 v65, v62, v60
	v_min_u32_e32 v60, v62, v60
	v_min_u32_e32 v36, v59, v36
	v_max_u32_e32 v59, v61, v43
	v_min_u32_e32 v43, v61, v43
	v_max_u32_e32 v61, v55, v37
	v_min_u32_e32 v37, v55, v37
	v_max_u32_e32 v62, v58, v42
	v_min_u32_e32 v42, v58, v42
	v_min_u32_e32 v58, v66, v63
	v_max_u32_e32 v67, v44, v60
	v_max_u32_e32 v55, v36, v35
	v_min_u32_e32 v35, v36, v35
	v_min_u32_e32 v36, v160, v57
	v_max_u32_e32 v161, v45, v37
	v_min_u32_e32 v44, v44, v60
	v_max_u32_e32 v60, v67, v58
	v_min_u32_e32 v58, v67, v58
	v_max_u32_e32 v67, v48, v56
	v_min_u32_e32 v48, v48, v56
	v_max_u32_e32 v56, v40, v42
	v_min_u32_e32 v37, v45, v37
	v_max_u32_e32 v45, v161, v36
	v_min_u32_e32 v36, v161, v36
	v_max_u32_e32 v161, v49, v43
	v_min_u32_e32 v43, v49, v43
	v_max_u32_e32 v49, v41, v35
	v_min_u32_e32 v40, v40, v42
	v_max_u32_e32 v42, v56, v48
	v_min_u32_e32 v48, v56, v48
	v_min_u32_e32 v35, v41, v35
	v_max_u32_e32 v41, v49, v43
	v_min_u32_e32 v43, v49, v43
	v_max_u32_e32 v56, v67, v60
	v_min_u32_e32 v60, v67, v60
	v_max_u32_e32 v67, v42, v58
	v_min_u32_e32 v42, v42, v58
	v_max_u32_e32 v58, v48, v44
	v_min_u32_e32 v44, v48, v44
	v_max_u32_e32 v48, v50, v64
	v_min_u32_e32 v50, v50, v64
	v_max_u32_e32 v64, v46, v62
	v_max_u32_e32 v49, v161, v45
	v_min_u32_e32 v45, v161, v45
	v_max_u32_e32 v161, v41, v36
	v_min_u32_e32 v36, v41, v36
	v_max_u32_e32 v41, v43, v37
	v_min_u32_e32 v37, v43, v37
	v_max_u32_e32 v43, v51, v59
	v_min_u32_e32 v51, v51, v59
	v_max_u32_e32 v59, v47, v55
	v_min_u32_e32 v46, v46, v62
	v_max_u32_e32 v62, v64, v50
	v_min_u32_e32 v50, v64, v50
	v_max_u32_e32 v64, v52, v65
	v_min_u32_e32 v52, v52, v65
	v_max_u32_e32 v65, v38, v54
	v_min_u32_e32 v47, v47, v55
	v_max_u32_e32 v55, v59, v51
	v_min_u32_e32 v51, v59, v51
	v_max_u32_e32 v59, v53, v61
	v_min_u32_e32 v53, v53, v61
	v_max_u32_e32 v61, v39, v34
	v_min_u32_e32 v38, v38, v54
	v_max_u32_e32 v54, v65, v52
	v_min_u32_e32 v52, v65, v52
	v_min_u32_e32 v34, v39, v34
	v_max_u32_e32 v39, v61, v53
	v_min_u32_e32 v53, v61, v53
	v_max_u32_e32 v65, v64, v62
	v_min_u32_e32 v62, v64, v62
	v_max_u32_e32 v64, v54, v50
	v_min_u32_e32 v50, v54, v50
	v_max_u32_e32 v54, v52, v46
	v_min_u32_e32 v46, v52, v46
	v_max_u32_e32 v61, v59, v55
	v_min_u32_e32 v55, v59, v55
	v_max_u32_e32 v59, v39, v51
	v_min_u32_e32 v39, v39, v51
	v_max_u32_e32 v51, v53, v47
	v_min_u32_e32 v47, v53, v47
	v_min_u32_e32 v52, v48, v56
	v_min_u32_e32 v68, v65, v60
	v_min_u32_e32 v69, v62, v67
	v_min_u32_e32 v96, v64, v42
	v_min_u32_e32 v97, v50, v58
	v_min_u32_e32 v158, v54, v44
	v_min_u32_e32 v159, v46, v40
	v_min_u32_e32 v53, v43, v49
	v_min_u32_e32 v162, v61, v45
	v_min_u32_e32 v163, v55, v161
	v_min_u32_e32 v164, v59, v36
	v_min_u32_e32 v165, v39, v41
	v_min_u32_e32 v166, v51, v37
	v_min_u32_e32 v167, v47, v35
	v_max3_u32 v34, v66, v63, v34
	v_max3_u32 v48, v48, v56, v167
	v_max3_u32 v35, v52, v47, v35
	v_max3_u32 v47, v65, v60, v166
	v_max3_u32 v37, v68, v51, v37
	v_max3_u32 v51, v62, v67, v165
	v_max3_u32 v39, v69, v39, v41
	v_max3_u32 v41, v64, v42, v164
	v_max3_u32 v36, v96, v59, v36
	v_max3_u32 v42, v50, v58, v163
	v_max3_u32 v50, v97, v55, v161
	v_max3_u32 v44, v54, v44, v162
	v_max3_u32 v45, v158, v61, v45
	v_max3_u32 v40, v46, v40, v53
	v_max3_u32 v43, v159, v43, v49
	v_max3_u32 v38, v38, v160, v57
	v_max_u32_e32 v46, v34, v36
	v_min_u32_e32 v34, v34, v36
	v_max_u32_e32 v36, v48, v42
	v_min_u32_e32 v42, v48, v42
; __device__ __forceinline__ void topk_phase(LAS unsigned char* lds, const bf16_t* qp, const bf16_t* keys, const float* SU, const float* SV, int* sel_e, float* sel_g, float* sel_su, int G, int b) {
;     ...
;             for (int i = 0; i < 16; ++i) T[p][i] = umax_(T[p][i], lo16[15 - i]);
;             SN_BITONIC16(T[p]);
;             TOPK_XMERGE(T[p], 16); TOPK_XMERGE(T[p], 32);
	v_max_u32_e32 v48, v35, v50
	v_min_u32_e32 v35, v35, v50
	v_max_u32_e32 v49, v47, v44
	v_min_u32_e32 v44, v47, v44
	v_max_u32_e32 v47, v37, v45
	v_min_u32_e32 v37, v37, v45
	v_max_u32_e32 v45, v51, v40
	v_min_u32_e32 v40, v51, v40
	v_max_u32_e32 v50, v39, v43
	v_min_u32_e32 v39, v39, v43
	v_max_u32_e32 v43, v41, v38
	v_min_u32_e32 v38, v41, v38
	v_max_u32_e32 v41, v46, v47
	v_min_u32_e32 v46, v46, v47
	v_max_u32_e32 v47, v36, v45
	v_min_u32_e32 v36, v36, v45
	v_max_u32_e32 v45, v48, v50
	v_min_u32_e32 v48, v48, v50
	v_max_u32_e32 v50, v49, v43
	v_min_u32_e32 v43, v49, v43
	v_max_u32_e32 v49, v34, v37
	v_min_u32_e32 v34, v34, v37
	v_max_u32_e32 v37, v42, v40
	v_min_u32_e32 v40, v42, v40
	v_max_u32_e32 v42, v35, v39
	v_min_u32_e32 v35, v35, v39
	v_max_u32_e32 v39, v44, v38
	v_min_u32_e32 v38, v44, v38
	v_max_u32_e32 v44, v41, v45
	v_min_u32_e32 v41, v41, v45
	v_max_u32_e32 v45, v47, v50
	v_min_u32_e32 v47, v47, v50
	v_max_u32_e32 v50, v46, v48
	v_min_u32_e32 v46, v46, v48
	v_max_u32_e32 v48, v36, v43
	v_min_u32_e32 v36, v36, v43
	v_max_u32_e32 v43, v49, v42
	v_min_u32_e32 v42, v49, v42
	v_max_u32_e32 v49, v37, v39
	v_min_u32_e32 v37, v37, v39
	v_max_u32_e32 v39, v34, v35
	v_min_u32_e32 v34, v34, v35
	v_max_u32_e32 v35, v40, v38
	v_min_u32_e32 v38, v40, v38
	v_max_u32_e32 v40, v44, v45
	v_min_u32_e32 v44, v44, v45
	v_max_u32_e32 v45, v41, v47
	v_min_u32_e32 v41, v41, v47
	v_max_u32_e32 v47, v50, v48
	v_min_u32_e32 v48, v50, v48
	v_max_u32_e32 v50, v46, v36
	v_min_u32_e32 v36, v46, v36
	v_max_u32_e32 v46, v43, v49
	v_min_u32_e32 v43, v43, v49
	v_max_u32_e32 v49, v42, v37
	v_min_u32_e32 v37, v42, v37
	v_max_u32_e32 v42, v39, v35
	v_min_u32_e32 v35, v39, v35
	v_max_u32_e32 v39, v34, v38
	v_min_u32_e32 v34, v34, v38
	v_mov_b32_e32 v38, v40
	v_mov_b32_e32 v51, v44
	v_mov_b32_e32 v52, v45
	v_mov_b32_e32 v53, v41
	v_mov_b32_e32 v54, v47
	v_mov_b32_e32 v55, v48
	v_mov_b32_e32 v56, v50
	v_mov_b32_e32 v57, v36
	v_mov_b32_e32 v58, v46
	v_mov_b32_e32 v59, v43
	v_mov_b32_e32 v60, v49
	v_mov_b32_e32 v61, v37
	v_mov_b32_e32 v62, v42
	v_mov_b32_e32 v63, v35
	v_mov_b32_e32 v64, v39
	v_mov_b32_e32 v65, v34
	v_permlane16_swap_b32_e32 v40, v38
	v_permlane16_swap_b32_e32 v44, v51
	v_permlane16_swap_b32_e32 v45, v52
	v_permlane16_swap_b32_e32 v41, v53
	v_permlane16_swap_b32_e32 v47, v54
	v_permlane16_swap_b32_e32 v48, v55
	v_permlane16_swap_b32_e32 v50, v56
	v_permlane16_swap_b32_e32 v36, v57
	v_permlane16_swap_b32_e32 v46, v58
	v_permlane16_swap_b32_e32 v43, v59
	v_permlane16_swap_b32_e32 v49, v60
	v_permlane16_swap_b32_e32 v37, v61
	v_permlane16_swap_b32_e32 v42, v62
	v_permlane16_swap_b32_e32 v35, v63
	v_permlane16_swap_b32_e32 v39, v64
	v_permlane16_swap_b32_e32 v34, v65
	v_max_u32_e32 v40, v40, v65
	v_max_u32_e32 v44, v44, v64
	v_max_u32_e32 v45, v45, v63
	v_max_u32_e32 v41, v41, v62
	v_max_u32_e32 v47, v47, v61
	v_max_u32_e32 v48, v48, v60
	v_max_u32_e32 v50, v50, v59
	v_max_u32_e32 v36, v36, v58
	v_max_u32_e32 v46, v46, v57
	v_max_u32_e32 v43, v43, v56
	v_max_u32_e32 v49, v49, v55
	v_max_u32_e32 v37, v37, v54
	v_max_u32_e32 v42, v42, v53
	v_max_u32_e32 v35, v35, v52
	v_max_u32_e32 v39, v39, v51
	v_max_u32_e32 v34, v34, v38
	v_max_u32_e32 v38, v40, v46
	v_min_u32_e32 v40, v40, v46
	v_max_u32_e32 v46, v44, v43
	v_min_u32_e32 v43, v44, v43
	v_max_u32_e32 v44, v45, v49
	v_min_u32_e32 v45, v45, v49
	v_max_u32_e32 v49, v41, v37
	v_min_u32_e32 v37, v41, v37
	v_max_u32_e32 v41, v47, v42
	v_min_u32_e32 v42, v47, v42
	v_max_u32_e32 v47, v48, v35
	v_min_u32_e32 v35, v48, v35
	v_max_u32_e32 v48, v50, v39
	v_min_u32_e32 v39, v50, v39
	v_max_u32_e32 v50, v36, v34
	v_min_u32_e32 v34, v36, v34
	v_max_u32_e32 v36, v38, v41
	v_min_u32_e32 v38, v38, v41
	v_max_u32_e32 v41, v46, v47
	v_min_u32_e32 v46, v46, v47
	v_max_u32_e32 v47, v44, v48
	v_min_u32_e32 v44, v44, v48
	v_max_u32_e32 v48, v49, v50
	v_min_u32_e32 v49, v49, v50
	v_max_u32_e32 v50, v40, v42
	v_min_u32_e32 v40, v40, v42
	v_max_u32_e32 v42, v43, v35
	v_min_u32_e32 v35, v43, v35
	v_max_u32_e32 v43, v45, v39
	v_min_u32_e32 v39, v45, v39
	v_max_u32_e32 v45, v37, v34
	v_min_u32_e32 v34, v37, v34
	v_max_u32_e32 v37, v36, v47
	v_min_u32_e32 v47, v36, v47
	v_max_u32_e32 v51, v41, v48
	v_min_u32_e32 v41, v41, v48
	v_max_u32_e32 v48, v38, v44
	v_min_u32_e32 v44, v38, v44
	v_max_u32_e32 v52, v46, v49
	v_min_u32_e32 v46, v46, v49
	v_max_u32_e32 v49, v50, v43
	v_min_u32_e32 v50, v50, v43
	v_max_u32_e32 v53, v42, v45
	v_min_u32_e32 v55, v42, v45
	v_max_u32_e32 v58, v40, v39
	v_min_u32_e32 v59, v40, v39
	v_max_u32_e32 v60, v35, v34
	v_min_u32_e32 v34, v35, v34
	v_max_u32_e32 v36, v37, v51
	v_min_u32_e32 v37, v37, v51
	v_max_u32_e32 v38, v47, v41
	v_min_u32_e32 v39, v47, v41
	v_max_u32_e32 v40, v48, v52
	v_min_u32_e32 v41, v48, v52
	v_max_u32_e32 v42, v44, v46
	v_min_u32_e32 v43, v44, v46
	v_max_u32_e32 v44, v49, v53
	v_min_u32_e32 v45, v49, v53
	v_max_u32_e32 v54, v50, v55
	v_min_u32_e32 v56, v50, v55
	v_max_u32_e32 v57, v58, v60
	v_min_u32_e32 v66, v58, v60
	v_max_u32_e32 v67, v59, v34
	v_min_u32_e32 v68, v59, v34
	v_mov_b32_e32 v69, v36
	v_mov_b32_e32 v158, v37
	v_mov_b32_e32 v159, v38
	v_mov_b32_e32 v160, v39
	v_mov_b32_e32 v161, v40
	v_mov_b32_e32 v162, v41
	v_mov_b32_e32 v163, v42
	v_mov_b32_e32 v97, v43
	v_mov_b32_e32 v53, v44
	v_mov_b32_e32 v52, v45
	v_mov_b32_e32 v51, v54
	v_mov_b32_e32 v50, v56
	v_mov_b32_e32 v49, v57
	v_mov_b32_e32 v48, v66
	v_mov_b32_e32 v47, v67
	v_mov_b32_e32 v46, v68
	v_permlane32_swap_b32_e32 v36, v69
	v_permlane32_swap_b32_e32 v37, v158
	v_permlane32_swap_b32_e32 v38, v159
	v_permlane32_swap_b32_e32 v39, v160
	v_permlane32_swap_b32_e32 v40, v161
	v_permlane32_swap_b32_e32 v41, v162
; __device__ __forceinline__ void topk_phase(LAS unsigned char* lds, const bf16_t* qp, const bf16_t* keys, const float* SU, const float* SV, int* sel_e, float* sel_g, float* sel_su, int G, int b) {
;     ...
;             TOPK_XMERGE(T[p], 16); TOPK_XMERGE(T[p], 32);
	v_permlane32_swap_b32_e32 v42, v163
	v_permlane32_swap_b32_e32 v43, v97
	v_permlane32_swap_b32_e32 v44, v53
	v_permlane32_swap_b32_e32 v45, v52
	v_permlane32_swap_b32_e32 v54, v51
	v_permlane32_swap_b32_e32 v56, v50
	v_permlane32_swap_b32_e32 v57, v49
	v_permlane32_swap_b32_e32 v66, v48
	v_permlane32_swap_b32_e32 v67, v47
	v_permlane32_swap_b32_e32 v68, v46
	v_max_u32_e32 v59, v70, v157
	v_max_u32_e32 v60, v71, v156
	v_max_u32_e32 v61, v72, v155
	v_max_u32_e32 v62, v73, v154
	v_max_u32_e32 v63, v74, v153
	v_max_u32_e32 v64, v75, v152
	v_max_u32_e32 v65, v76, v151
	v_max_u32_e32 v70, v77, v150
	v_max_u32_e32 v71, v134, v149
	v_max_u32_e32 v72, v135, v148
	v_max_u32_e32 v73, v136, v147
	v_max_u32_e32 v74, v137, v146
	v_max_u32_e32 v75, v138, v145
	v_max_u32_e32 v76, v139, v144
	v_max_u32_e32 v77, v140, v143
	v_max_u32_e32 v96, v141, v142
	v_max_u32_e32 v55, v59, v71
	v_max_u32_e32 v135, v60, v72
	v_max_u32_e32 v136, v61, v73
	v_max_u32_e32 v137, v62, v74
	v_max_u32_e32 v138, v63, v75
	v_max_u32_e32 v139, v64, v76
	v_max_u32_e32 v140, v65, v77
	v_max_u32_e32 v141, v70, v96
	v_max_u32_e32 v46, v36, v46
	v_max_u32_e32 v47, v37, v47
	v_max_u32_e32 v48, v38, v48
	v_max_u32_e32 v49, v39, v49
	v_max_u32_e32 v50, v40, v50
	v_max_u32_e32 v51, v41, v51
	v_max_u32_e32 v52, v42, v52
	v_max_u32_e32 v53, v43, v53
	v_max_u32_e32 v97, v44, v97
	v_max_u32_e32 v134, v45, v163
	v_max_u32_e32 v143, v54, v162
	v_max_u32_e32 v149, v56, v161
	v_max_u32_e32 v150, v57, v160
	v_max_u32_e32 v151, v66, v159
	v_max_u32_e32 v152, v67, v158
	v_max_u32_e32 v153, v68, v69
	v_max_u32_e32 v216, v59, v71
	v_min_u32_e32 v224, v59, v71
	v_max_u32_e32 v217, v60, v72
	v_min_u32_e32 v225, v60, v72
	v_max_u32_e32 v218, v61, v73
	v_min_u32_e32 v226, v61, v73
	v_max_u32_e32 v219, v62, v74
	v_min_u32_e32 v227, v62, v74
	v_max_u32_e32 v220, v63, v75
	v_min_u32_e32 v228, v63, v75
	v_max_u32_e32 v221, v64, v76
	v_min_u32_e32 v229, v64, v76
	v_max_u32_e32 v222, v65, v77
	v_min_u32_e32 v230, v65, v77
	v_max_u32_e32 v223, v70, v96
	v_min_u32_e32 v231, v70, v96
	v_max_u32_e32 v232, v216, v220
	v_min_u32_e32 v236, v216, v220
	v_max_u32_e32 v233, v217, v221
	v_min_u32_e32 v237, v217, v221
	v_max_u32_e32 v234, v218, v222
	v_min_u32_e32 v238, v218, v222
	v_max_u32_e32 v235, v219, v223
	v_min_u32_e32 v239, v219, v223
	v_max_u32_e32 v240, v224, v228
	v_min_u32_e32 v246, v224, v228
	v_max_u32_e32 v241, v225, v229
	v_min_u32_e32 v247, v225, v229
	v_max_u32_e32 v244, v226, v230
	v_min_u32_e32 v248, v226, v230
	v_max_u32_e32 v245, v227, v231
	v_min_u32_e32 v249, v227, v231
	v_max_u32_e32 v216, v232, v234
	v_min_u32_e32 v218, v232, v234
	v_max_u32_e32 v217, v233, v235
	v_min_u32_e32 v219, v233, v235
	v_max_u32_e32 v220, v236, v238
	v_min_u32_e32 v222, v236, v238
	v_max_u32_e32 v221, v237, v239
	v_min_u32_e32 v223, v237, v239
	v_max_u32_e32 v224, v240, v244
	v_min_u32_e32 v226, v240, v244
	v_max_u32_e32 v225, v241, v245
	v_min_u32_e32 v227, v241, v245
	v_max_u32_e32 v228, v246, v248
	v_min_u32_e32 v230, v246, v248
	v_max_u32_e32 v229, v247, v249
	v_min_u32_e32 v231, v247, v249
	v_max_u32_e32 v34, v216, v217
	v_min_u32_e32 v35, v216, v217
	v_max_u32_e32 v36, v218, v219
	v_min_u32_e32 v37, v218, v219
	v_max_u32_e32 v54, v220, v221
	v_min_u32_e32 v55, v220, v221
	v_max_u32_e32 v56, v222, v223
	v_min_u32_e32 v57, v222, v223
	v_max_u32_e32 v58, v224, v225
	v_min_u32_e32 v59, v224, v225
	v_max_u32_e32 v60, v226, v227
	v_min_u32_e32 v61, v226, v227
	v_max_u32_e32 v62, v228, v229
	v_min_u32_e32 v63, v228, v229
	v_max_u32_e32 v64, v230, v231
	v_min_u32_e32 v65, v230, v231
	v_max_u32_e32 v216, v46, v97
	v_min_u32_e32 v224, v46, v97
	v_max_u32_e32 v217, v47, v134
	v_min_u32_e32 v225, v47, v134
	v_max_u32_e32 v218, v48, v143
	v_min_u32_e32 v226, v48, v143
	v_max_u32_e32 v219, v49, v149
	v_min_u32_e32 v227, v49, v149
	v_max_u32_e32 v220, v50, v150
	v_min_u32_e32 v228, v50, v150
	v_max_u32_e32 v221, v51, v151
	v_min_u32_e32 v229, v51, v151
	v_max_u32_e32 v222, v52, v152
	v_min_u32_e32 v230, v52, v152
	v_max_u32_e32 v223, v53, v153
	v_min_u32_e32 v231, v53, v153
	v_max_u32_e32 v232, v216, v220
	v_min_u32_e32 v236, v216, v220
	v_max_u32_e32 v233, v217, v221
	v_min_u32_e32 v237, v217, v221
	v_max_u32_e32 v234, v218, v222
	v_min_u32_e32 v238, v218, v222
	v_max_u32_e32 v235, v219, v223
	v_min_u32_e32 v239, v219, v223
	v_max_u32_e32 v240, v224, v228
	v_min_u32_e32 v246, v224, v228
	v_max_u32_e32 v241, v225, v229
	v_min_u32_e32 v247, v225, v229
	v_max_u32_e32 v244, v226, v230
	v_min_u32_e32 v248, v226, v230
	v_max_u32_e32 v245, v227, v231
	v_min_u32_e32 v249, v227, v231
	v_max_u32_e32 v216, v232, v234
	v_min_u32_e32 v218, v232, v234
	v_max_u32_e32 v217, v233, v235
	v_min_u32_e32 v219, v233, v235
	v_max_u32_e32 v220, v236, v238
	v_min_u32_e32 v222, v236, v238
	v_max_u32_e32 v221, v237, v239
	v_min_u32_e32 v223, v237, v239
	v_max_u32_e32 v224, v240, v244
	v_min_u32_e32 v226, v240, v244
	v_max_u32_e32 v225, v241, v245
	v_min_u32_e32 v227, v241, v245
	v_max_u32_e32 v228, v246, v248
	v_min_u32_e32 v230, v246, v248
	v_max_u32_e32 v229, v247, v249
	v_min_u32_e32 v231, v247, v249
	v_max_u32_e32 v38, v216, v217
	v_min_u32_e32 v39, v216, v217
	v_max_u32_e32 v40, v218, v219
	v_min_u32_e32 v41, v218, v219
	v_max_u32_e32 v42, v220, v221
	v_min_u32_e32 v43, v220, v221
	v_max_u32_e32 v44, v222, v223
	v_min_u32_e32 v45, v222, v223
	v_max_u32_e32 v46, v224, v225
	v_min_u32_e32 v47, v224, v225
	v_max_u32_e32 v48, v226, v227
	v_min_u32_e32 v49, v226, v227
	v_max_u32_e32 v50, v228, v229
	v_min_u32_e32 v51, v228, v229
	v_max_u32_e32 v52, v230, v231
	v_min_u32_e32 v53, v230, v231
	v_ashrrev_i32_e32 v216, 31, v34
	v_ashrrev_i32_e32 v217, 31, v35
; __device__ __forceinline__ unsigned mono(float f) { const unsigned u = __float_as_uint(f); return (u & 0x80000000u) ? ~u : (u ^ 0x80000000u); }
; __device__ __forceinline__ float unmono(unsigned u) { return __uint_as_float((u & 0x80000000u) ? (u ^ 0x80000000u) : ~u); }
; __device__ __forceinline__ void topk_phase(LAS unsigned char* lds, const bf16_t* qp, const bf16_t* keys, const float* SU, const float* SV, int* sel_e, float* sel_g, float* sel_su, int G, int b) {
;     ...
;         float v1[16], v2[16];
; #pragma unroll
;         for (int i = 0; i < 16; ++i) { v1[i] = unmono(T[0][i] & ~127u); v2[i] = unmono(T[1][i] & ~127u); }
;         unsigned ck[16];
; #pragma unroll
;         for (int sidx = 0; sidx < 13; ++sidx) {
;             unsigned keyk[4];
; #pragma unroll
;             for (int k = 0; k < 4; ++k) {
;                 const int c = 4 * sidx + k;
;                 if (c < 50) { const int ci = cand_i(c), cj = cand_j(c); keyk[k] = (mono(v1[ci] + v2[cj]) & ~255u) | (unsigned)(255 - (ci * 16 + cj)); }
;                 else keyk[k] = 0u;
;             }
;             ck[sidx] = fq == 0 ? keyk[0] : fq == 1 ? keyk[1] : fq == 2 ? keyk[2] : keyk[3];
;         }
	v_ashrrev_i32_e32 v218, 31, v36
	v_ashrrev_i32_e32 v219, 31, v37
	v_ashrrev_i32_e32 v220, 31, v54
	v_ashrrev_i32_e32 v221, 31, v55
	v_ashrrev_i32_e32 v222, 31, v56
	v_ashrrev_i32_e32 v223, 31, v57
	v_ashrrev_i32_e32 v224, 31, v58
	v_ashrrev_i32_e32 v225, 31, v59
	v_ashrrev_i32_e32 v226, 31, v60
	v_ashrrev_i32_e32 v227, 31, v61
	v_ashrrev_i32_e32 v228, 31, v62
	v_ashrrev_i32_e32 v229, 31, v63
	v_ashrrev_i32_e32 v230, 31, v64
	v_ashrrev_i32_e32 v231, 31, v65
	v_bitop3_b32 v170, v34, v216, s12 bitop3:0x93
	v_bitop3_b32 v171, v35, v217, s12 bitop3:0x93
	v_bitop3_b32 v172, v36, v218, s12 bitop3:0x93
	v_bitop3_b32 v173, v37, v219, s12 bitop3:0x93
	v_bitop3_b32 v174, v54, v220, s12 bitop3:0x93
	v_bitop3_b32 v175, v55, v221, s12 bitop3:0x93
	v_bitop3_b32 v176, v56, v222, s12 bitop3:0x93
	v_bitop3_b32 v177, v57, v223, s12 bitop3:0x93
	v_bitop3_b32 v178, v58, v224, s12 bitop3:0x93
	v_bitop3_b32 v179, v59, v225, s12 bitop3:0x93
	v_bitop3_b32 v180, v60, v226, s12 bitop3:0x93
	v_bitop3_b32 v181, v61, v227, s12 bitop3:0x93
	v_bitop3_b32 v182, v62, v228, s12 bitop3:0x93
	v_bitop3_b32 v183, v63, v229, s12 bitop3:0x93
	v_bitop3_b32 v184, v64, v230, s12 bitop3:0x93
	v_bitop3_b32 v185, v65, v231, s12 bitop3:0x93
	v_ashrrev_i32_e32 v216, 31, v38
	v_ashrrev_i32_e32 v217, 31, v39
	v_ashrrev_i32_e32 v218, 31, v40
	v_ashrrev_i32_e32 v219, 31, v41
	v_ashrrev_i32_e32 v220, 31, v42
	v_ashrrev_i32_e32 v221, 31, v43
	v_ashrrev_i32_e32 v222, 31, v44
	v_ashrrev_i32_e32 v223, 31, v45
	v_ashrrev_i32_e32 v224, 31, v46
	v_ashrrev_i32_e32 v225, 31, v47
	v_ashrrev_i32_e32 v226, 31, v48
	v_ashrrev_i32_e32 v227, 31, v49
	v_ashrrev_i32_e32 v228, 31, v50
	v_ashrrev_i32_e32 v229, 31, v51
	v_ashrrev_i32_e32 v230, 31, v52
	v_ashrrev_i32_e32 v231, 31, v53
	v_bitop3_b32 v186, v38, v216, s12 bitop3:0x93
	v_bitop3_b32 v187, v39, v217, s12 bitop3:0x93
	v_bitop3_b32 v188, v40, v218, s12 bitop3:0x93
	v_bitop3_b32 v189, v41, v219, s12 bitop3:0x93
	v_bitop3_b32 v190, v42, v220, s12 bitop3:0x93
	v_bitop3_b32 v191, v43, v221, s12 bitop3:0x93
	v_bitop3_b32 v192, v44, v222, s12 bitop3:0x93
	v_bitop3_b32 v193, v45, v223, s12 bitop3:0x93
	v_bitop3_b32 v194, v46, v224, s12 bitop3:0x93
	v_bitop3_b32 v195, v47, v225, s12 bitop3:0x93
	v_bitop3_b32 v196, v48, v226, s12 bitop3:0x93
	v_bitop3_b32 v197, v49, v227, s12 bitop3:0x93
	v_bitop3_b32 v198, v50, v228, s12 bitop3:0x93
	v_bitop3_b32 v199, v51, v229, s12 bitop3:0x93
	v_bitop3_b32 v200, v52, v230, s12 bitop3:0x93
	v_bitop3_b32 v201, v53, v231, s12 bitop3:0x93
	v_cndmask_b32_e64 v250, v186, v187, s[16:17]
	v_cndmask_b32_e64 v250, v250, v188, s[18:19]
	v_cndmask_b32_e64 v250, v250, v189, s[20:21]
	v_cndmask_b32_e64 v251, v190, v191, s[16:17]
	v_cndmask_b32_e64 v251, v251, v192, s[18:19]
	v_cndmask_b32_e64 v251, v251, v193, s[20:21]
	v_cndmask_b32_e64 v252, v194, v195, s[16:17]
	v_cndmask_b32_e64 v252, v252, v196, s[18:19]
	v_cndmask_b32_e64 v252, v252, v197, s[20:21]
	v_cndmask_b32_e64 v253, v198, v199, s[16:17]
	v_cndmask_b32_e64 v253, v253, v200, s[18:19]
	v_cndmask_b32_e64 v253, v253, v201, s[20:21]
	v_add_f32_e32 v254, v170, v250
	v_ashrrev_i32_e32 v255, 31, v254
	v_bitop3_b32 v254, v254, v255, v132 bitop3:0x1e
	v_and_or_b32 v68, v254, s60, v203
	v_add_f32_e32 v254, v170, v251
	v_ashrrev_i32_e32 v255, 31, v254
	v_bitop3_b32 v254, v254, v255, v132 bitop3:0x1e
	v_and_or_b32 v69, v254, s60, v204
	v_add_f32_e32 v254, v170, v252
	v_ashrrev_i32_e32 v255, 31, v254
	v_bitop3_b32 v254, v254, v255, v132 bitop3:0x1e
	v_and_or_b32 v97, v254, s60, v205
	v_add_f32_e32 v254, v170, v253
	v_ashrrev_i32_e32 v255, 31, v254
	v_bitop3_b32 v254, v254, v255, v132 bitop3:0x1e
	v_and_or_b32 v134, v254, s60, v206
	v_add_f32_e32 v254, v171, v250
	v_ashrrev_i32_e32 v255, 31, v254
	v_bitop3_b32 v254, v254, v255, v132 bitop3:0x1e
	v_and_or_b32 v142, v254, s60, v207
	v_add_f32_e32 v254, v171, v251
	v_ashrrev_i32_e32 v255, 31, v254
	v_bitop3_b32 v254, v254, v255, v132 bitop3:0x1e
	v_and_or_b32 v143, v254, s60, v208
	v_add_f32_e32 v254, v172, v250
	v_ashrrev_i32_e32 v255, 31, v254
	v_bitop3_b32 v254, v254, v255, v132 bitop3:0x1e
	v_and_or_b32 v144, v254, s60, v209
	v_cndmask_b32_e64 v232, v172, v173, s[16:17]
	v_cndmask_b32_e64 v232, v232, v173, s[22:23]
	v_cndmask_b32_e64 v233, v190, v186, s[16:17]
	v_cndmask_b32_e64 v233, v233, v187, s[18:19]
	v_cndmask_b32_e64 v233, v233, v188, s[20:21]
	v_add_f32_e32 v254, v232, v233
	v_ashrrev_i32_e32 v255, 31, v254
	v_bitop3_b32 v254, v254, v255, v132 bitop3:0x1e
	v_and_or_b32 v145, v254, s60, v210
	v_cndmask_b32_e64 v234, v173, v174, s[16:17]
	v_cndmask_b32_e64 v234, v234, v174, s[22:23]
	v_cndmask_b32_e64 v235, v189, v186, s[16:17]
	v_cndmask_b32_e64 v235, v235, v187, s[18:19]
	v_cndmask_b32_e64 v235, v235, v188, s[20:21]
	v_add_f32_e32 v254, v234, v235
	v_ashrrev_i32_e32 v255, 31, v254
	v_bitop3_b32 v254, v254, v255, v132 bitop3:0x1e
	v_and_or_b32 v135, v254, s60, v211
	v_cndmask_b32_e64 v236, v175, v176, s[22:23]
	v_cndmask_b32_e64 v237, v186, v187, s[24:25]
	v_add_f32_e32 v254, v236, v237
	v_ashrrev_i32_e32 v255, 31, v254
	v_bitop3_b32 v254, v254, v255, v132 bitop3:0x1e
	v_and_or_b32 v136, v254, s60, v212
	v_cndmask_b32_e64 v238, v177, v178, s[18:19]
	v_cndmask_b32_e64 v238, v238, v179, s[20:21]
	v_cndmask_b32_e64 v239, v186, v187, s[16:17]
	v_add_f32_e32 v254, v238, v239
	v_ashrrev_i32_e32 v255, 31, v254
	v_bitop3_b32 v254, v254, v255, v132 bitop3:0x1e
	v_and_or_b32 v70, v254, s60, v213
	v_cndmask_b32_e64 v240, v180, v181, s[16:17]
	v_cndmask_b32_e64 v240, v240, v182, s[18:19]
	v_cndmask_b32_e64 v240, v240, v183, s[20:21]
	v_add_f32_e32 v254, v240, v186
	v_ashrrev_i32_e32 v255, 31, v254
	v_bitop3_b32 v254, v254, v255, v132 bitop3:0x1e
; __device__ __forceinline__ unsigned mono(float f) { const unsigned u = __float_as_uint(f); return (u & 0x80000000u) ? ~u : (u ^ 0x80000000u); }
; __device__ __forceinline__ void topk_phase(LAS unsigned char* lds, const bf16_t* qp, const bf16_t* keys, const float* SU, const float* SV, int* sel_e, float* sel_g, float* sel_su, int G, int b) {
;     ...
;                 const int c = 4 * sidx + k;
;                 if (c < 50) { const int ci = cand_i(c), cj = cand_j(c); keyk[k] = (mono(v1[ci] + v2[cj]) & ~255u) | (unsigned)(255 - (ci * 16 + cj)); }
;                 else keyk[k] = 0u;
;             }
;             ck[sidx] = fq == 0 ? keyk[0] : fq == 1 ? keyk[1] : fq == 2 ? keyk[2] : keyk[3];
;         }
;         ck[13] = 0u; ck[14] = 0u; ck[15] = 0u;
;         SN_SORT16(ck);
;         TOPK_XMERGE(ck, 16); TOPK_XMERGE(ck, 32);
	v_and_or_b32 v71, v254, s60, v214
	v_cndmask_b32_e64 v241, v184, v185, s[16:17]
	v_add_f32_e32 v254, v241, v186
	v_ashrrev_i32_e32 v255, 31, v254
	v_bitop3_b32 v254, v254, v255, v132 bitop3:0x1e
	v_and_or_b32 v67, v254, s60, v215
	v_cndmask_b32_e64 v67, v67, 0, s[22:23]
	v_max_u32_e32 v66, v68, v69
	v_min_u32_e32 v68, v68, v69
	v_max_u32_e32 v69, v97, v134
	v_min_u32_e32 v72, v97, v134
	v_max_u32_e32 v73, v66, v69
	v_min_u32_e32 v66, v66, v69
	v_max_u32_e32 v69, v68, v72
	v_min_u32_e32 v68, v68, v72
	v_max_u32_e32 v72, v69, v66
	v_min_u32_e32 v66, v69, v66
	v_max_u32_e32 v69, v142, v143
	v_min_u32_e32 v74, v142, v143
	v_max_u32_e32 v75, v144, v145
	v_min_u32_e32 v76, v144, v145
	v_max_u32_e32 v77, v69, v75
	v_min_u32_e32 v69, v69, v75
	v_max_u32_e32 v75, v74, v76
	v_min_u32_e32 v74, v74, v76
	v_max_u32_e32 v76, v75, v69
	v_min_u32_e32 v69, v75, v69
	v_max_u32_e32 v75, v73, v77
	v_min_u32_e32 v73, v73, v77
	v_max_u32_e32 v77, v66, v69
	v_min_u32_e32 v66, v66, v69
	v_max_u32_e32 v69, v77, v73
	v_min_u32_e32 v73, v77, v73
	v_max_u32_e32 v77, v72, v76
	v_min_u32_e32 v72, v72, v76
	v_max_u32_e32 v76, v68, v74
	v_min_u32_e32 v68, v68, v74
	v_max_u32_e32 v74, v76, v72
	v_min_u32_e32 v72, v76, v72
	v_max_u32_e32 v76, v77, v69
	v_min_u32_e32 v69, v77, v69
	v_max_u32_e32 v77, v74, v73
	v_min_u32_e32 v73, v74, v73
	v_max_u32_e32 v74, v72, v66
	v_min_u32_e32 v66, v72, v66
	v_max_u32_e32 v72, v135, v136
	v_min_u32_e32 v96, v135, v136
	v_max_u32_e32 v97, v70, v71
	v_min_u32_e32 v70, v70, v71
	v_max_u32_e32 v71, v72, v97
	v_min_u32_e32 v72, v72, v97
	v_max_u32_e32 v97, v96, v70
	v_min_u32_e32 v134, v97, v72
	v_max_u32_e32 v135, v71, v67
	v_min_u32_e32 v67, v71, v67
	v_min_u32_e32 v70, v96, v70
	v_max_u32_e32 v71, v134, v67
	v_min_u32_e32 v134, v134, v67
	v_max_u32_e32 v96, v97, v72
	v_med3_u32 v67, v97, v72, v67
	v_max_u32_e32 v72, v70, v134
	v_min_u32_e32 v70, v70, v134
	v_max_u32_e32 v71, v96, v71
	v_max_u32_e32 v96, v75, v135
	v_min_u32_e32 v75, v75, v135
	v_max_u32_e32 v97, v73, v70
	v_min_u32_e32 v70, v73, v70
	v_max_u32_e32 v73, v97, v75
	v_min_u32_e32 v75, v97, v75
	v_max_u32_e32 v97, v69, v67
	v_min_u32_e32 v67, v69, v67
	v_max_u32_e32 v69, v66, v67
	v_min_u32_e32 v66, v66, v67
	v_max_u32_e32 v67, v97, v73
	v_min_u32_e32 v73, v97, v73
	v_max_u32_e32 v97, v69, v75
	v_min_u32_e32 v69, v69, v75
	v_max_u32_e32 v75, v66, v70
	v_min_u32_e32 v66, v66, v70
	v_max_u32_e32 v70, v76, v71
	v_min_u32_e32 v71, v76, v71
	v_max_u32_e32 v76, v74, v71
	v_min_u32_e32 v71, v74, v71
	v_max_u32_e32 v74, v77, v72
	v_min_u32_e32 v72, v77, v72
	v_max_u32_e32 v77, v68, v72
	v_min_u32_e32 v68, v68, v72
	v_max_u32_e32 v72, v74, v76
	v_min_u32_e32 v74, v74, v76
	v_max_u32_e32 v76, v77, v71
	v_min_u32_e32 v71, v77, v71
	v_max_u32_e32 v77, v70, v67
	v_min_u32_e32 v67, v70, v67
	v_max_u32_e32 v70, v72, v73
	v_min_u32_e32 v72, v72, v73
	v_max_u32_e32 v73, v74, v97
	v_min_u32_e32 v74, v74, v97
	v_max_u32_e32 v97, v76, v69
	v_min_u32_e32 v69, v76, v69
	v_max_u32_e32 v76, v71, v75
	v_min_u32_e32 v71, v71, v75
	v_max_u32_e32 v75, v68, v66
	v_min_u32_e32 v66, v68, v66
	v_mov_b32_e32 v68, v96
	v_mov_b32_e32 v134, v77
	v_mov_b32_e32 v135, v67
	v_mov_b32_e32 v136, v70
	v_mov_b32_e32 v137, v72
	v_mov_b32_e32 v138, v73
	v_mov_b32_e32 v139, v74
	v_mov_b32_e32 v140, v97
	v_mov_b32_e32 v141, v69
	v_mov_b32_e32 v142, v76
	v_mov_b32_e32 v143, v71
	v_mov_b32_e32 v144, v75
	v_mov_b32_e32 v145, v66
	v_mov_b32_e32 v146, 0
	v_mov_b32_e32 v147, 0
	v_permlane16_swap_b32_e32 v96, v68
	v_permlane16_swap_b32_e32 v77, v134
	v_permlane16_swap_b32_e32 v67, v135
	v_permlane16_swap_b32_e32 v70, v136
	v_permlane16_swap_b32_e32 v72, v137
	v_permlane16_swap_b32_e32 v73, v138
	v_permlane16_swap_b32_e32 v74, v139
	v_permlane16_swap_b32_e32 v97, v140
	v_permlane16_swap_b32_e32 v69, v141
	v_permlane16_swap_b32_e32 v76, v142
	v_permlane16_swap_b32_e32 v71, v143
; __device__ __forceinline__ void topk_phase(LAS unsigned char* lds, const bf16_t* qp, const bf16_t* keys, const float* SU, const float* SV, int* sel_e, float* sel_g, float* sel_su, int G, int b) {
;     ...
;         SN_SORT16(ck);
;         TOPK_XMERGE(ck, 16); TOPK_XMERGE(ck, 32);
;         if (fq == 0) {
; #pragma unroll
;             for (int i = 0; i < 16; ++i) { wl[i] = T[0][i]; wl[16 + i] = T[1][i]; }
;         }
	v_permlane16_swap_b32_e32 v75, v144
	v_permlane16_swap_b32_e32 v66, v145
	v_permlane16_swap_b32_e32 v146, v147
	v_max_u32_e32 v96, v96, v147
	v_max_u32_e32 v77, v77, v147
	v_max_u32_e32 v67, v67, v147
	v_max_u32_e32 v70, v70, v145
	v_max_u32_e32 v72, v72, v144
	v_max_u32_e32 v73, v73, v143
	v_max_u32_e32 v74, v74, v142
	v_max_u32_e32 v97, v97, v141
	v_max_u32_e32 v69, v69, v140
	v_max_u32_e32 v76, v76, v139
	v_max_u32_e32 v71, v71, v138
	v_max_u32_e32 v75, v75, v137
	v_max_u32_e32 v66, v66, v136
	v_max_u32_e32 v135, v146, v135
	v_max_u32_e32 v134, v146, v134
	v_max_u32_e32 v68, v146, v68
	v_max_u32_e32 v136, v96, v69
	v_min_u32_e32 v69, v96, v69
	v_max_u32_e32 v96, v77, v76
	v_min_u32_e32 v76, v77, v76
	v_max_u32_e32 v77, v67, v71
	v_min_u32_e32 v67, v67, v71
	v_max_u32_e32 v71, v70, v75
	v_min_u32_e32 v70, v70, v75
	v_max_u32_e32 v75, v72, v66
	v_min_u32_e32 v66, v72, v66
	v_max_u32_e32 v72, v73, v135
	v_min_u32_e32 v73, v73, v135
	v_max_u32_e32 v135, v74, v134
	v_min_u32_e32 v74, v74, v134
	v_max_u32_e32 v134, v97, v68
	v_min_u32_e32 v68, v97, v68
	v_max_u32_e32 v97, v136, v75
	v_min_u32_e32 v75, v136, v75
	v_max_u32_e32 v136, v96, v72
	v_min_u32_e32 v72, v96, v72
	v_max_u32_e32 v96, v77, v135
	v_min_u32_e32 v77, v77, v135
	v_max_u32_e32 v135, v71, v134
	v_min_u32_e32 v71, v71, v134
	v_max_u32_e32 v134, v69, v66
	v_min_u32_e32 v66, v69, v66
	v_max_u32_e32 v69, v76, v73
	v_min_u32_e32 v73, v76, v73
	v_max_u32_e32 v76, v67, v74
	v_min_u32_e32 v67, v67, v74
	v_max_u32_e32 v74, v70, v68
	v_min_u32_e32 v68, v70, v68
	v_max_u32_e32 v70, v97, v96
	v_min_u32_e32 v96, v97, v96
	v_max_u32_e32 v97, v136, v135
	v_min_u32_e32 v135, v136, v135
	v_max_u32_e32 v136, v75, v77
	v_min_u32_e32 v75, v75, v77
	v_max_u32_e32 v77, v72, v71
	v_min_u32_e32 v137, v72, v71
	v_max_u32_e32 v138, v134, v76
	v_min_u32_e32 v134, v134, v76
	v_max_u32_e32 v76, v69, v74
	v_min_u32_e32 v139, v69, v74
	v_max_u32_e32 v140, v66, v67
	v_min_u32_e32 v141, v66, v67
	v_max_u32_e32 v142, v73, v68
	v_min_u32_e32 v143, v73, v68
	v_max_u32_e32 v66, v70, v97
	v_min_u32_e32 v67, v70, v97
	v_max_u32_e32 v68, v96, v135
	v_min_u32_e32 v69, v96, v135
	v_max_u32_e32 v70, v136, v77
	v_min_u32_e32 v71, v136, v77
	v_max_u32_e32 v72, v75, v137
	v_min_u32_e32 v73, v75, v137
	v_max_u32_e32 v74, v138, v76
	v_min_u32_e32 v75, v138, v76
	v_max_u32_e32 v76, v134, v139
	v_min_u32_e32 v77, v134, v139
	v_max_u32_e32 v96, v140, v142
	v_min_u32_e32 v97, v140, v142
	v_max_u32_e32 v134, v141, v143
	v_min_u32_e32 v135, v141, v143
	v_mov_b32_e32 v136, v66
	v_mov_b32_e32 v137, v67
	v_mov_b32_e32 v138, v68
	v_mov_b32_e32 v139, v69
	v_mov_b32_e32 v140, v70
	v_mov_b32_e32 v141, v71
	v_mov_b32_e32 v142, v72
	v_mov_b32_e32 v143, v73
	v_mov_b32_e32 v144, v74
	v_mov_b32_e32 v145, v75
	v_mov_b32_e32 v146, v76
	v_mov_b32_e32 v147, v77
	v_mov_b32_e32 v148, v96
	v_mov_b32_e32 v149, v97
	v_mov_b32_e32 v150, v134
	v_mov_b32_e32 v151, v135
	v_permlane32_swap_b32_e32 v66, v136
	v_permlane32_swap_b32_e32 v67, v137
	v_permlane32_swap_b32_e32 v68, v138
	v_permlane32_swap_b32_e32 v69, v139
	v_permlane32_swap_b32_e32 v70, v140
	v_permlane32_swap_b32_e32 v71, v141
	v_permlane32_swap_b32_e32 v72, v142
	v_permlane32_swap_b32_e32 v73, v143
	v_permlane32_swap_b32_e32 v74, v144
	v_permlane32_swap_b32_e32 v75, v145
	v_permlane32_swap_b32_e32 v76, v146
	v_permlane32_swap_b32_e32 v77, v147
	v_permlane32_swap_b32_e32 v96, v148
	v_permlane32_swap_b32_e32 v97, v149
	v_permlane32_swap_b32_e32 v134, v150
	v_permlane32_swap_b32_e32 v135, v151
	s_and_saveexec_b64 s[0:1], s[40:41]
	s_cbranch_execz .LBB0_739
	ds_write_b128 v83, v[34:37]
	ds_write_b128 v83, v[38:41] offset:64
	ds_write_b128 v83, v[54:57] offset:16
	ds_write_b128 v83, v[42:45] offset:80
	ds_write_b128 v83, v[58:61] offset:32
	ds_write_b128 v83, v[46:49] offset:96
	ds_write_b128 v83, v[62:65] offset:48
	ds_write_b128 v83, v[50:53] offset:112
